# v17 + sc1 (write-through) on the P7 (x1), P10 (act) and P11 (Y) epilogue stores so that the grid barrier's L2 write-back finds less dirty data
# speedup vs baseline: 1.0173x; 1.0169x over previous
.LBB0_1150:
	v_lshl_or_b32 v6, s71, 8, v202
	v_ashrrev_i32_e32 v7, 31, v6
	v_add_u32_e32 v10, s70, v200
	v_lshl_add_u64 v[8:9], v[6:7], 2, s[14:15]
	v_ashrrev_i32_e32 v11, 31, v10
	global_load_dwordx4 v[16:19], v[8:9], off
	global_load_dwordx4 v[20:23], v[8:9], off offset:64
	global_load_dwordx4 v[24:27], v[8:9], off offset:512
	global_load_dwordx4 v[28:31], v[8:9], off offset:576
	v_lshlrev_b64 v[10:11], 11, v[10:11]
	v_lshl_add_u64 v[6:7], v[10:11], 0, v[6:7]
	v_lshlrev_b32_e32 v14, 2, v6
	global_load_dwordx4 v[212:215], v14, s[6:7] nt
	global_load_dwordx4 v[216:219], v14, s[6:7] offset:64 nt
	global_load_dwordx4 v[220:223], v14, s[6:7] offset:512 nt
	global_load_dwordx4 v[224:227], v14, s[6:7] offset:576 nt
	v_add_u32_e32 v12, s24, v14
	global_load_dwordx4 v[228:231], v12, s[6:7] nt
	global_load_dwordx4 v[232:235], v12, s[6:7] offset:64 nt
	global_load_dwordx4 v[236:239], v12, s[6:7] offset:512 nt
	global_load_dwordx4 v[240:243], v12, s[6:7] offset:576 nt
	v_add_u32_e32 v12, s10, v14
	global_load_dwordx4 v[244:247], v12, s[6:7] nt
	global_load_dwordx4 v[248:251], v12, s[6:7] offset:64 nt
	global_load_dwordx4 v[2:5], v12, s[6:7] offset:512 nt
	global_load_dwordx4 v[8:11], v12, s[6:7] offset:576 nt
	s_andn2_b64 vcc, exec, s[0:1]
	s_mov_b64 s[0:1], -1
	s_nop 15
	s_waitcnt vmcnt(12)
	v_pk_mul_f32 v[16:17], v[16:17], s[22:23] op_sel_hi:[1,0]
	v_pk_mul_f32 v[18:19], v[18:19], s[22:23] op_sel_hi:[1,0]
	v_pk_mul_f32 v[20:21], v[20:21], s[22:23] op_sel_hi:[1,0]
	v_pk_mul_f32 v[22:23], v[22:23], s[22:23] op_sel_hi:[1,0]
	v_pk_mul_f32 v[24:25], v[24:25], s[22:23] op_sel_hi:[1,0]
	v_pk_mul_f32 v[26:27], v[26:27], s[22:23] op_sel_hi:[1,0]
	v_pk_mul_f32 v[28:29], v[28:29], s[22:23] op_sel_hi:[1,0]
	v_pk_mul_f32 v[30:31], v[30:31], s[22:23] op_sel_hi:[1,0]
	s_waitcnt vmcnt(8)
	v_pk_fma_f32 v[214:215], v[160:161], v[18:19], v[214:215]
	v_pk_fma_f32 v[212:213], v[158:159], v[16:17], v[212:213]
	v_pk_fma_f32 v[218:219], v[156:157], v[22:23], v[218:219]
	v_pk_fma_f32 v[216:217], v[154:155], v[20:21], v[216:217]
	v_pk_fma_f32 v[222:223], v[152:153], v[26:27], v[222:223]
	v_pk_fma_f32 v[220:221], v[150:151], v[24:25], v[220:221]
	v_pk_fma_f32 v[226:227], v[140:141], v[30:31], v[226:227]
	v_pk_fma_f32 v[224:225], v[138:139], v[28:29], v[224:225]
	global_store_dwordx4 v14, v[212:215], s[48:49] sc1
	global_store_dwordx4 v14, v[216:219], s[48:49] offset:64 sc1
	global_store_dwordx4 v14, v[220:223], s[48:49] offset:512 sc1
	global_store_dwordx4 v14, v[224:227], s[48:49] offset:576 sc1
	v_add_u32_e32 v12, s26, v14
	global_load_dwordx4 v[212:215], v12, s[6:7] nt
	global_load_dwordx4 v[216:219], v12, s[6:7] offset:64 nt
	global_load_dwordx4 v[220:223], v12, s[6:7] offset:512 nt
	global_load_dwordx4 v[224:227], v12, s[6:7] offset:576 nt
	s_waitcnt vmcnt(8)
	v_pk_fma_f32 v[230:231], v[148:149], v[18:19], v[230:231]
	v_pk_fma_f32 v[228:229], v[146:147], v[16:17], v[228:229]
	v_pk_fma_f32 v[234:235], v[144:145], v[22:23], v[234:235]
	v_pk_fma_f32 v[232:233], v[142:143], v[20:21], v[232:233]
	v_pk_fma_f32 v[238:239], v[136:137], v[26:27], v[238:239]
	v_pk_fma_f32 v[236:237], v[134:135], v[24:25], v[236:237]
	v_pk_fma_f32 v[242:243], v[124:125], v[30:31], v[242:243]
	v_pk_fma_f32 v[240:241], v[122:123], v[28:29], v[240:241]
	v_add_u32_e32 v13, s24, v14
	global_store_dwordx4 v13, v[228:231], s[48:49] sc1
	global_store_dwordx4 v13, v[232:235], s[48:49] offset:64 sc1
	global_store_dwordx4 v13, v[236:239], s[48:49] offset:512 sc1
	global_store_dwordx4 v13, v[240:243], s[48:49] offset:576 sc1
	v_add_u32_e32 v12, s28, v14
	global_load_dwordx4 v[228:231], v12, s[6:7] nt
	global_load_dwordx4 v[232:235], v12, s[6:7] offset:64 nt
	global_load_dwordx4 v[236:239], v12, s[6:7] offset:512 nt
	global_load_dwordx4 v[240:243], v12, s[6:7] offset:576 nt
	s_waitcnt vmcnt(8)
	v_pk_fma_f32 v[246:247], v[132:133], v[18:19], v[246:247]
	v_pk_fma_f32 v[244:245], v[130:131], v[16:17], v[244:245]
	v_pk_fma_f32 v[250:251], v[128:129], v[22:23], v[250:251]
	v_pk_fma_f32 v[248:249], v[126:127], v[20:21], v[248:249]
	v_pk_fma_f32 v[4:5], v[120:121], v[26:27], v[4:5]
	v_pk_fma_f32 v[2:3], v[118:119], v[24:25], v[2:3]
	v_pk_fma_f32 v[10:11], v[108:109], v[30:31], v[10:11]
	v_pk_fma_f32 v[8:9], v[106:107], v[28:29], v[8:9]
	v_add_u32_e32 v13, s10, v14
	global_store_dwordx4 v13, v[244:247], s[48:49] sc1
	global_store_dwordx4 v13, v[248:251], s[48:49] offset:64 sc1
	global_store_dwordx4 v13, v[2:5], s[48:49] offset:512 sc1
	global_store_dwordx4 v13, v[8:11], s[48:49] offset:576 sc1
	v_add_u32_e32 v12, s30, v14
	global_load_dwordx4 v[244:247], v12, s[6:7] nt
	global_load_dwordx4 v[248:251], v12, s[6:7] offset:64 nt
	global_load_dwordx4 v[2:5], v12, s[6:7] offset:512 nt
	global_load_dwordx4 v[8:11], v12, s[6:7] offset:576 nt
	s_waitcnt vmcnt(8)
	v_pk_fma_f32 v[214:215], v[116:117], v[18:19], v[214:215]
	v_pk_fma_f32 v[212:213], v[114:115], v[16:17], v[212:213]
	v_pk_fma_f32 v[218:219], v[112:113], v[22:23], v[218:219]
	v_pk_fma_f32 v[216:217], v[110:111], v[20:21], v[216:217]
	v_pk_fma_f32 v[222:223], v[104:105], v[26:27], v[222:223]
	v_pk_fma_f32 v[220:221], v[102:103], v[24:25], v[220:221]
	v_pk_fma_f32 v[226:227], v[100:101], v[30:31], v[226:227]
	v_pk_fma_f32 v[224:225], v[98:99], v[28:29], v[224:225]
	v_add_u32_e32 v13, s26, v14
	global_store_dwordx4 v13, v[212:215], s[48:49] sc1
	global_store_dwordx4 v13, v[216:219], s[48:49] offset:64 sc1
	global_store_dwordx4 v13, v[220:223], s[48:49] offset:512 sc1
	global_store_dwordx4 v13, v[224:227], s[48:49] offset:576 sc1
	v_add_u32_e32 v12, s34, v14
	global_load_dwordx4 v[212:215], v12, s[6:7] nt
	global_load_dwordx4 v[216:219], v12, s[6:7] offset:64 nt
	global_load_dwordx4 v[220:223], v12, s[6:7] offset:512 nt
	global_load_dwordx4 v[224:227], v12, s[6:7] offset:576 nt
	s_waitcnt vmcnt(8)
	v_pk_fma_f32 v[230:231], v[96:97], v[18:19], v[230:231]
	v_pk_fma_f32 v[228:229], v[94:95], v[16:17], v[228:229]
	v_pk_fma_f32 v[234:235], v[92:93], v[22:23], v[234:235]
	v_pk_fma_f32 v[232:233], v[90:91], v[20:21], v[232:233]
	v_pk_fma_f32 v[238:239], v[88:89], v[26:27], v[238:239]
	v_pk_fma_f32 v[236:237], v[86:87], v[24:25], v[236:237]
	v_pk_fma_f32 v[242:243], v[76:77], v[30:31], v[242:243]
	v_pk_fma_f32 v[240:241], v[74:75], v[28:29], v[240:241]
	v_add_u32_e32 v13, s28, v14
	global_store_dwordx4 v13, v[228:231], s[48:49] sc1
	global_store_dwordx4 v13, v[232:235], s[48:49] offset:64 sc1
	global_store_dwordx4 v13, v[236:239], s[48:49] offset:512 sc1
	global_store_dwordx4 v13, v[240:243], s[48:49] offset:576 sc1
	v_add_u32_e32 v12, s36, v14
	global_load_dwordx4 v[228:231], v12, s[6:7] nt
	global_load_dwordx4 v[232:235], v12, s[6:7] offset:64 nt
	global_load_dwordx4 v[236:239], v12, s[6:7] offset:512 nt
	global_load_dwordx4 v[240:243], v12, s[6:7] offset:576 nt
	s_waitcnt vmcnt(8)
	v_pk_fma_f32 v[246:247], v[84:85], v[18:19], v[246:247]
	v_pk_fma_f32 v[244:245], v[82:83], v[16:17], v[244:245]
	v_pk_fma_f32 v[250:251], v[80:81], v[22:23], v[250:251]
	v_pk_fma_f32 v[248:249], v[78:79], v[20:21], v[248:249]
	v_pk_fma_f32 v[4:5], v[72:73], v[26:27], v[4:5]
	v_pk_fma_f32 v[2:3], v[70:71], v[24:25], v[2:3]
	v_pk_fma_f32 v[10:11], v[60:61], v[30:31], v[10:11]
	v_pk_fma_f32 v[8:9], v[58:59], v[28:29], v[8:9]
	v_add_u32_e32 v13, s30, v14
	global_store_dwordx4 v13, v[244:247], s[48:49] sc1
	global_store_dwordx4 v13, v[248:251], s[48:49] offset:64 sc1
	global_store_dwordx4 v13, v[2:5], s[48:49] offset:512 sc1
	global_store_dwordx4 v13, v[8:11], s[48:49] offset:576 sc1
	s_waitcnt vmcnt(4)
	v_pk_fma_f32 v[214:215], v[68:69], v[18:19], v[214:215]
	v_pk_fma_f32 v[212:213], v[66:67], v[16:17], v[212:213]
	v_pk_fma_f32 v[218:219], v[64:65], v[22:23], v[218:219]
	v_pk_fma_f32 v[216:217], v[62:63], v[20:21], v[216:217]
	v_pk_fma_f32 v[222:223], v[56:57], v[26:27], v[222:223]
	v_pk_fma_f32 v[220:221], v[54:55], v[24:25], v[220:221]
	v_pk_fma_f32 v[226:227], v[44:45], v[30:31], v[226:227]
	v_pk_fma_f32 v[224:225], v[42:43], v[28:29], v[224:225]
	v_add_u32_e32 v13, s34, v14
	global_store_dwordx4 v13, v[212:215], s[48:49] sc1
	global_store_dwordx4 v13, v[216:219], s[48:49] offset:64 sc1
	global_store_dwordx4 v13, v[220:223], s[48:49] offset:512 sc1
	global_store_dwordx4 v13, v[224:227], s[48:49] offset:576 sc1
	s_waitcnt vmcnt(0)
	v_pk_fma_f32 v[230:231], v[52:53], v[18:19], v[230:231]
	v_pk_fma_f32 v[228:229], v[50:51], v[16:17], v[228:229]
	v_pk_fma_f32 v[234:235], v[48:49], v[22:23], v[234:235]
	v_pk_fma_f32 v[232:233], v[46:47], v[20:21], v[232:233]
	v_pk_fma_f32 v[238:239], v[40:41], v[26:27], v[238:239]
	v_pk_fma_f32 v[236:237], v[38:39], v[24:25], v[236:237]
	v_pk_fma_f32 v[242:243], v[36:37], v[30:31], v[242:243]
	v_pk_fma_f32 v[240:241], v[34:35], v[28:29], v[240:241]
	v_add_u32_e32 v13, s36, v14
	global_store_dwordx4 v13, v[228:231], s[48:49] sc1
	global_store_dwordx4 v13, v[232:235], s[48:49] offset:64 sc1
	global_store_dwordx4 v13, v[236:239], s[48:49] offset:512 sc1
	global_store_dwordx4 v13, v[240:243], s[48:49] offset:576 sc1
	s_cbranch_vccnz .LBB0_1134
	s_andn2_b64 vcc, exec, s[12:13]
	s_cbranch_vccnz .LBB0_1133
	s_barrier
	s_branch .LBB0_1133

.LBB0_1677:
	v_mov_b32_e32 v2, v238
	s_add_u32 s0, s79, 0xffffff00
	s_nop 15
	s_nop 15
	s_nop 15
	s_addc_u32 s1, s80, -1
	v_lshlrev_b32_e32 v3, 5, v2
	v_ashrrev_i32_e32 v4, 1, v2
	v_and_b32_e32 v3, 0x1e0, v3
	v_and_b32_e32 v5, -8, v4
	s_add_i32 s2, s33, s69
	v_add3_u32 v8, s53, v3, v5
	v_add_u32_e32 v10, s2, v4
	v_pk_mul_f32 v[4:5], v[190:191], s[28:29] op_sel_hi:[1,0]
	v_lshlrev_b32_e32 v2, 4, v2
	v_mul_f32_e32 v6, 0xbfb8aa3b, v4
	v_exp_f32_e32 v16, v6
	v_mul_f32_e32 v27, 0xbfb8aa3b, v5
	v_exp_f32_e32 v27, v27
	v_add_u32_e32 v9, s53, v2
	v_add_f32_e32 v22, 1.0, v16
	v_and_b32_e32 v11, 16, v2
	v_pk_mul_f32 v[2:3], v[192:193], s[28:29] op_sel_hi:[1,0]
	v_pk_mul_f32 v[16:17], v[158:159], s[30:31] op_sel_hi:[1,0]
	v_add_f32_e32 v25, 1.0, v27
	v_rcp_f32_e32 v23, v22
	s_nop 0
	v_mul_f32_e32 v4, v4, v23
	v_mul_f32_e32 v23, 0xbfb8aa3b, v2
	v_exp_f32_e32 v23, v23
	v_mul_f32_e32 v4, v4, v16
	v_add_f32_e32 v23, 1.0, v23
	v_mul_f32_e32 v22, 0xbfb8aa3b, v3
	v_rcp_f32_e32 v16, v25
	s_nop 0
	v_mul_f32_e32 v5, v5, v16
	v_exp_f32_e32 v22, v22
	v_mul_f32_e32 v5, v5, v17
	v_add_f32_e32 v22, 1.0, v22
	v_pk_mul_f32 v[14:15], v[160:161], s[30:31] op_sel_hi:[1,0]
	v_rcp_f32_e32 v16, v23
	s_nop 0
	v_mul_f32_e32 v2, v2, v16
	v_mul_f32_e32 v14, v2, v14
	v_pk_mul_f32 v[12:13], v[186:187], s[28:29] op_sel_hi:[1,0]
	v_rcp_f32_e32 v2, v22
	s_nop 0
	v_mul_f32_e32 v2, v3, v2
	v_mul_f32_e32 v3, v2, v15
	v_mul_f32_e32 v2, 0xbfb8aa3b, v12
	v_exp_f32_e32 v15, v2
	v_med3_f32 v4, v4, s75, v239
	v_med3_f32 v5, v5, s75, v239
	v_mov_b32_e32 v2, v203
	v_cvt_pk_fp8_f32 v2, v4, v5
	v_add_f32_e32 v4, 1.0, v15
	v_med3_f32 v14, v14, s75, v239
	v_med3_f32 v3, v3, s75, v239
	v_cvt_pk_fp8_f32 v2, v14, v3 op_sel:[0,0,1]
	v_mul_f32_e32 v16, 0xbfb8aa3b, v13
	v_exp_f32_e32 v16, v16
	s_nop 0
	v_add_f32_e32 v5, 1.0, v16
	v_pk_mul_f32 v[6:7], v[188:189], s[28:29] op_sel_hi:[1,0]
	v_mul_f32_e32 v14, 0xbfb8aa3b, v6
	v_exp_f32_e32 v14, v14
	v_rcp_f32_e32 v3, v4
	s_nop 0
	v_mul_f32_e32 v3, v12, v3
	v_add_f32_e32 v14, 1.0, v14
	v_rcp_f32_e32 v4, v5
	s_nop 0
	v_mul_f32_e32 v4, v13, v4
	v_mul_f32_e32 v13, 0xbfb8aa3b, v7
	v_exp_f32_e32 v13, v13
	s_nop 0
	v_add_f32_e32 v13, 1.0, v13
	v_rcp_f32_e32 v5, v14
	s_nop 0
	v_mul_f32_e32 v5, v6, v5
	v_pk_mul_f32 v[20:21], v[154:155], s[30:31] op_sel_hi:[1,0]
	v_mul_f32_e32 v3, v3, v20
	v_mul_f32_e32 v4, v4, v21
	v_pk_mul_f32 v[18:19], v[156:157], s[30:31] op_sel_hi:[1,0]
	v_rcp_f32_e32 v6, v13
	s_nop 0
	v_mul_f32_e32 v6, v7, v6
	v_med3_f32 v7, v3, s75, v239
	v_med3_f32 v4, v4, s75, v239
	v_mov_b32_e32 v3, v203
	v_cvt_pk_fp8_f32 v3, v7, v4
	v_mul_f32_e32 v4, v6, v19
	v_pk_mul_f32 v[6:7], v[182:183], s[28:29] op_sel_hi:[1,0]
	v_mul_f32_e32 v5, v5, v18
	v_mul_f32_e32 v12, 0xbfb8aa3b, v6
	v_exp_f32_e32 v18, v12
	v_mul_f32_e32 v29, 0xbfb8aa3b, v7
	v_exp_f32_e32 v29, v29
	v_med3_f32 v5, v5, s75, v239
	v_add_f32_e32 v24, 1.0, v18
	v_med3_f32 v4, v4, s75, v239
	v_cvt_pk_fp8_f32 v3, v5, v4 op_sel:[0,0,1]
	v_pk_mul_f32 v[4:5], v[184:185], s[28:29] op_sel_hi:[1,0]
	v_add_f32_e32 v27, 1.0, v29
	v_rcp_f32_e32 v25, v24
	s_nop 0
	v_mul_f32_e32 v6, v6, v25
	v_mul_f32_e32 v25, 0xbfb8aa3b, v4
	v_pk_mul_f32 v[18:19], v[150:151], s[30:31] op_sel_hi:[1,0]
	v_exp_f32_e32 v25, v25
	v_mul_f32_e32 v6, v6, v18
	v_add_f32_e32 v25, 1.0, v25
	v_mul_f32_e32 v24, 0xbfb8aa3b, v5
	v_rcp_f32_e32 v18, v27
	s_nop 0
	v_mul_f32_e32 v7, v7, v18
	v_exp_f32_e32 v24, v24
	v_mul_f32_e32 v7, v7, v19
	v_add_f32_e32 v24, 1.0, v24
	v_pk_mul_f32 v[16:17], v[152:153], s[30:31] op_sel_hi:[1,0]
	v_rcp_f32_e32 v18, v25
	s_nop 0
	v_mul_f32_e32 v4, v4, v18
	v_mul_f32_e32 v16, v4, v16
	v_pk_mul_f32 v[14:15], v[178:179], s[28:29] op_sel_hi:[1,0]
	v_rcp_f32_e32 v4, v24
	s_nop 0
	v_mul_f32_e32 v4, v5, v4
	v_mul_f32_e32 v5, v4, v17
	v_mul_f32_e32 v4, 0xbfb8aa3b, v14
	v_exp_f32_e32 v17, v4
	v_med3_f32 v6, v6, s75, v239
	v_med3_f32 v7, v7, s75, v239
	v_mov_b32_e32 v4, v203
	v_cvt_pk_fp8_f32 v4, v6, v7
	v_add_f32_e32 v6, 1.0, v17
	v_med3_f32 v16, v16, s75, v239
	v_med3_f32 v5, v5, s75, v239
	v_cvt_pk_fp8_f32 v4, v16, v5 op_sel:[0,0,1]
	v_mul_f32_e32 v18, 0xbfb8aa3b, v15
	v_exp_f32_e32 v18, v18
	s_nop 0
	v_add_f32_e32 v7, 1.0, v18
	v_pk_mul_f32 v[12:13], v[180:181], s[28:29] op_sel_hi:[1,0]
	v_mul_f32_e32 v16, 0xbfb8aa3b, v12
	v_exp_f32_e32 v16, v16
	v_rcp_f32_e32 v5, v6
	s_nop 0
	v_mul_f32_e32 v5, v14, v5
	v_add_f32_e32 v16, 1.0, v16
	v_rcp_f32_e32 v6, v7
	s_nop 0
	v_mul_f32_e32 v6, v15, v6
	v_mul_f32_e32 v15, 0xbfb8aa3b, v13
	v_exp_f32_e32 v15, v15
	s_nop 0
	v_add_f32_e32 v15, 1.0, v15
	v_rcp_f32_e32 v7, v16
	s_nop 0
	v_mul_f32_e32 v7, v12, v7
	v_pk_mul_f32 v[22:23], v[146:147], s[30:31] op_sel_hi:[1,0]
	v_mul_f32_e32 v5, v5, v22
	v_mul_f32_e32 v6, v6, v23
	v_pk_mul_f32 v[20:21], v[148:149], s[30:31] op_sel_hi:[1,0]
	v_rcp_f32_e32 v12, v15
	s_nop 0
	v_mul_f32_e32 v12, v13, v12
	v_med3_f32 v13, v5, s75, v239
	v_med3_f32 v6, v6, s75, v239
	v_mov_b32_e32 v5, v203
	v_cvt_pk_fp8_f32 v5, v13, v6
	v_mul_f32_e32 v6, v12, v21
	v_pk_mul_f32 v[12:13], v[174:175], s[28:29] op_sel_hi:[1,0]
	v_mul_f32_e32 v7, v7, v20
	v_mul_f32_e32 v14, 0xbfb8aa3b, v12
	v_exp_f32_e32 v20, v14
	v_mul_f32_e32 v31, 0xbfb8aa3b, v13
	v_exp_f32_e32 v31, v31
	v_med3_f32 v7, v7, s75, v239
	v_add_f32_e32 v26, 1.0, v20
	v_med3_f32 v6, v6, s75, v239
	v_cvt_pk_fp8_f32 v5, v7, v6 op_sel:[0,0,1]
	v_lshl_or_b32 v6, s18, 7, v11
	v_add_f32_e32 v29, 1.0, v31
	v_or_b32_e32 v11, s70, v6
	v_pk_mul_f32 v[6:7], v[176:177], s[28:29] op_sel_hi:[1,0]
	v_rcp_f32_e32 v27, v26
	s_nop 0
	v_mul_f32_e32 v12, v12, v27
	v_mul_f32_e32 v27, 0xbfb8aa3b, v6
	v_pk_mul_f32 v[20:21], v[142:143], s[30:31] op_sel_hi:[1,0]
	v_exp_f32_e32 v27, v27
	v_mul_f32_e32 v12, v12, v20
	v_add_f32_e32 v27, 1.0, v27
	v_mul_f32_e32 v26, 0xbfb8aa3b, v7
	v_rcp_f32_e32 v20, v29
	s_nop 0
	v_mul_f32_e32 v13, v13, v20
	v_exp_f32_e32 v26, v26
	v_mul_f32_e32 v13, v13, v21
	v_add_f32_e32 v26, 1.0, v26
	v_pk_mul_f32 v[18:19], v[144:145], s[30:31] op_sel_hi:[1,0]
	v_rcp_f32_e32 v20, v27
	s_nop 0
	v_mul_f32_e32 v6, v6, v20
	v_mul_f32_e32 v18, v6, v18
	v_pk_mul_f32 v[16:17], v[170:171], s[28:29] op_sel_hi:[1,0]
	v_rcp_f32_e32 v6, v26
	s_nop 0
	v_mul_f32_e32 v6, v7, v6
	v_mul_f32_e32 v7, v6, v19
	v_mul_f32_e32 v6, 0xbfb8aa3b, v16
	v_exp_f32_e32 v19, v6
	v_med3_f32 v12, v12, s75, v239
	v_med3_f32 v13, v13, s75, v239
	v_mov_b32_e32 v6, v203
	v_cvt_pk_fp8_f32 v6, v12, v13
	v_add_f32_e32 v12, 1.0, v19
	v_med3_f32 v18, v18, s75, v239
	v_med3_f32 v7, v7, s75, v239
	v_cvt_pk_fp8_f32 v6, v18, v7 op_sel:[0,0,1]
	v_mul_f32_e32 v20, 0xbfb8aa3b, v17
	v_exp_f32_e32 v20, v20
	s_nop 0
	v_add_f32_e32 v13, 1.0, v20
	v_pk_mul_f32 v[14:15], v[172:173], s[28:29] op_sel_hi:[1,0]
	v_mul_f32_e32 v18, 0xbfb8aa3b, v14
	v_exp_f32_e32 v18, v18
	v_rcp_f32_e32 v7, v12
	s_nop 0
	v_mul_f32_e32 v7, v16, v7
	v_add_f32_e32 v18, 1.0, v18
	v_rcp_f32_e32 v12, v13
	s_nop 0
	v_mul_f32_e32 v12, v17, v12
	v_mul_f32_e32 v17, 0xbfb8aa3b, v15
	v_exp_f32_e32 v17, v17
	s_nop 0
	v_add_f32_e32 v17, 1.0, v17
	v_rcp_f32_e32 v13, v18
	s_nop 0
	v_mul_f32_e32 v13, v14, v13
	v_pk_mul_f32 v[24:25], v[138:139], s[30:31] op_sel_hi:[1,0]
	v_mul_f32_e32 v7, v7, v24
	v_mul_f32_e32 v12, v12, v25
	v_pk_mul_f32 v[22:23], v[140:141], s[30:31] op_sel_hi:[1,0]
	v_rcp_f32_e32 v14, v17
	s_nop 0
	v_mul_f32_e32 v14, v15, v14
	v_med3_f32 v15, v7, s75, v239
	v_med3_f32 v12, v12, s75, v239
	v_mov_b32_e32 v7, v203
	v_cvt_pk_fp8_f32 v7, v15, v12
	v_mul_f32_e32 v12, v14, v23
	v_pk_mul_f32 v[14:15], v[166:167], s[28:29] op_sel_hi:[1,0]
	v_mul_f32_e32 v13, v13, v22
	v_mul_f32_e32 v16, 0xbfb8aa3b, v14
	v_exp_f32_e32 v22, v16
	v_mul_f32_e32 v33, 0xbfb8aa3b, v15
	v_exp_f32_e32 v33, v33
	v_med3_f32 v13, v13, s75, v239
	v_add_f32_e32 v28, 1.0, v22
	v_med3_f32 v12, v12, s75, v239
	v_cvt_pk_fp8_f32 v7, v13, v12 op_sel:[0,0,1]
	v_pk_mul_f32 v[12:13], v[168:169], s[28:29] op_sel_hi:[1,0]
	s_waitcnt lgkmcnt(0)
	v_add_f32_e32 v31, 1.0, v33
	v_rcp_f32_e32 v29, v28
	s_nop 0
	v_mul_f32_e32 v14, v14, v29
	v_mul_f32_e32 v29, 0xbfb8aa3b, v12
	v_pk_mul_f32 v[22:23], v[134:135], s[30:31] op_sel_hi:[1,0]
	v_exp_f32_e32 v29, v29
	v_mul_f32_e32 v14, v14, v22
	v_add_f32_e32 v29, 1.0, v29
	v_mul_f32_e32 v28, 0xbfb8aa3b, v13
	v_rcp_f32_e32 v22, v31
	s_nop 0
	v_mul_f32_e32 v15, v15, v22
	v_exp_f32_e32 v28, v28
	v_mul_f32_e32 v15, v15, v23
	v_add_f32_e32 v28, 1.0, v28
	v_pk_mul_f32 v[20:21], v[136:137], s[30:31] op_sel_hi:[1,0]
	v_rcp_f32_e32 v22, v29
	s_nop 0
	v_mul_f32_e32 v12, v12, v22
	v_mul_f32_e32 v20, v12, v20
	v_pk_mul_f32 v[18:19], v[162:163], s[28:29] op_sel_hi:[1,0]
	v_rcp_f32_e32 v12, v28
	s_nop 0
	v_mul_f32_e32 v12, v13, v12
	v_mul_f32_e32 v13, v12, v21
	v_mul_f32_e32 v12, 0xbfb8aa3b, v18
	v_exp_f32_e32 v21, v12
	v_med3_f32 v14, v14, s75, v239
	v_med3_f32 v15, v15, s75, v239
	v_mov_b32_e32 v12, v203
	v_cvt_pk_fp8_f32 v12, v14, v15
	v_add_f32_e32 v14, 1.0, v21
	v_med3_f32 v20, v20, s75, v239
	v_med3_f32 v13, v13, s75, v239
	v_cvt_pk_fp8_f32 v12, v20, v13 op_sel:[0,0,1]
	v_mul_f32_e32 v22, 0xbfb8aa3b, v19
	v_exp_f32_e32 v22, v22
	s_nop 0
	v_add_f32_e32 v15, 1.0, v22
	v_pk_mul_f32 v[16:17], v[164:165], s[28:29] op_sel_hi:[1,0]
	v_mul_f32_e32 v20, 0xbfb8aa3b, v16
	v_exp_f32_e32 v20, v20
	v_rcp_f32_e32 v13, v14
	s_nop 0
	v_mul_f32_e32 v13, v18, v13
	v_add_f32_e32 v20, 1.0, v20
	v_rcp_f32_e32 v14, v15
	s_nop 0
	v_mul_f32_e32 v14, v19, v14
	v_mul_f32_e32 v19, 0xbfb8aa3b, v17
	v_exp_f32_e32 v19, v19
	s_nop 0
	v_add_f32_e32 v19, 1.0, v19
	v_rcp_f32_e32 v15, v20
	s_nop 0
	v_mul_f32_e32 v15, v16, v15
	v_pk_mul_f32 v[26:27], v[130:131], s[30:31] op_sel_hi:[1,0]
	v_mul_f32_e32 v13, v13, v26
	v_mul_f32_e32 v14, v14, v27
	v_rcp_f32_e32 v16, v19
	s_nop 0
	v_mul_f32_e32 v16, v17, v16
	v_med3_f32 v17, v13, s75, v239
	v_med3_f32 v14, v14, s75, v239
	v_mov_b32_e32 v13, v203
	v_cvt_pk_fp8_f32 v13, v17, v14
	ds_write_b64 v8, v[2:3]
	ds_write_b64 v8, v[4:5] offset:512
	v_pk_mul_f32 v[24:25], v[132:133], s[30:31] op_sel_hi:[1,0]
	ds_read_b128 v[2:5], v9
	v_mul_f32_e32 v15, v15, v24
	v_mul_f32_e32 v14, v16, v25
	v_med3_f32 v15, v15, s75, v239
	v_med3_f32 v14, v14, s75, v239
	v_cvt_pk_fp8_f32 v13, v15, v14 op_sel:[0,0,1]
	v_lshl_add_u32 v10, v10, 9, v11
	s_waitcnt lgkmcnt(0)
	global_store_dwordx4 v10, v[2:5], s[16:17] sc1
	ds_write_b64 v8, v[6:7] offset:1024
	ds_write_b64 v8, v[12:13] offset:1536
	v_pk_mul_f32 v[12:13], v[126:127], s[28:29] op_sel_hi:[1,0]
	v_pk_mul_f32 v[6:7], v[128:129], s[28:29] op_sel_hi:[1,0]
	v_mul_f32_e32 v11, 0xbfb8aa3b, v12
	v_exp_f32_e32 v11, v11
	v_mul_f32_e32 v30, 0xbfb8aa3b, v13
	v_exp_f32_e32 v30, v30
	v_pk_mul_f32 v[20:21], v[94:95], s[30:31] op_sel_hi:[1,0]
	v_add_f32_e32 v11, 1.0, v11
	v_pk_mul_f32 v[18:19], v[96:97], s[30:31] op_sel_hi:[1,0]
	v_pk_mul_f32 v[16:17], v[122:123], s[28:29] op_sel_hi:[1,0]
	v_pk_mul_f32 v[14:15], v[124:125], s[28:29] op_sel_hi:[1,0]
	v_add_f32_e32 v28, 1.0, v30
	v_rcp_f32_e32 v11, v11
	s_nop 0
	v_mul_f32_e32 v11, v12, v11
	v_mul_f32_e32 v26, 0xbfb8aa3b, v6
	v_exp_f32_e32 v26, v26
	v_mul_f32_e32 v11, v20, v11
	v_add_f32_e32 v26, 1.0, v26
	v_rcp_f32_e32 v12, v28
	s_nop 0
	v_mul_f32_e32 v12, v13, v12
	v_mul_f32_e32 v12, v21, v12
	v_mul_f32_e32 v21, 0xbfb8aa3b, v7
	v_exp_f32_e32 v21, v21
	s_nop 0
	v_add_f32_e32 v21, 1.0, v21
	v_rcp_f32_e32 v13, v26
	s_nop 0
	v_mul_f32_e32 v6, v6, v13
	v_mul_f32_e32 v13, v18, v6
	v_rcp_f32_e32 v6, v21
	s_nop 0
	v_mul_f32_e32 v6, v7, v6
	v_mul_f32_e32 v7, v19, v6
	v_mul_f32_e32 v6, 0xbfb8aa3b, v16
	v_exp_f32_e32 v18, v6
	v_med3_f32 v11, v11, s75, v239
	v_med3_f32 v12, v12, s75, v239
	v_mov_b32_e32 v6, v203
	v_cvt_pk_fp8_f32 v6, v11, v12
	v_add_f32_e32 v11, 1.0, v18
	v_med3_f32 v13, v13, s75, v239
	v_med3_f32 v7, v7, s75, v239
	v_cvt_pk_fp8_f32 v6, v13, v7 op_sel:[0,0,1]
	v_mul_f32_e32 v19, 0xbfb8aa3b, v17
	v_exp_f32_e32 v19, v19
	s_nop 0
	v_add_f32_e32 v12, 1.0, v19
	v_rcp_f32_e32 v7, v11
	s_nop 0
	v_mul_f32_e32 v7, v16, v7
	v_mul_f32_e32 v16, 0xbfb8aa3b, v14
	v_exp_f32_e32 v16, v16
	s_nop 0
	v_add_f32_e32 v16, 1.0, v16
	v_rcp_f32_e32 v11, v12
	s_nop 0
	v_mul_f32_e32 v11, v17, v11
	v_mul_f32_e32 v17, 0xbfb8aa3b, v15
	v_exp_f32_e32 v17, v17
	s_nop 0
	v_add_f32_e32 v17, 1.0, v17
	v_rcp_f32_e32 v12, v16
	s_nop 0
	v_mul_f32_e32 v12, v14, v12
	v_pk_mul_f32 v[24:25], v[90:91], s[30:31] op_sel_hi:[1,0]
	v_mul_f32_e32 v7, v24, v7
	v_mul_f32_e32 v11, v25, v11
	v_med3_f32 v14, v7, s75, v239
	v_med3_f32 v11, v11, s75, v239
	v_mov_b32_e32 v7, v203
	v_cvt_pk_fp8_f32 v7, v14, v11
	v_pk_mul_f32 v[22:23], v[92:93], s[30:31] op_sel_hi:[1,0]
	v_rcp_f32_e32 v13, v17
	s_nop 0
	v_mul_f32_e32 v13, v15, v13
	v_mul_f32_e32 v12, v22, v12
	v_mul_f32_e32 v11, v23, v13
	v_med3_f32 v12, v12, s75, v239
	v_med3_f32 v11, v11, s75, v239
	v_pk_mul_f32 v[14:15], v[118:119], s[28:29] op_sel_hi:[1,0]
	v_cvt_pk_fp8_f32 v7, v12, v11 op_sel:[0,0,1]
	v_mul_f32_e32 v11, 0xbfb8aa3b, v14
	v_exp_f32_e32 v11, v11
	v_mul_f32_e32 v32, 0xbfb8aa3b, v15
	v_exp_f32_e32 v32, v32
	v_pk_mul_f32 v[12:13], v[120:121], s[28:29] op_sel_hi:[1,0]
	v_add_f32_e32 v11, 1.0, v11
	v_pk_mul_f32 v[22:23], v[86:87], s[30:31] op_sel_hi:[1,0]
	v_pk_mul_f32 v[20:21], v[88:89], s[30:31] op_sel_hi:[1,0]
	v_pk_mul_f32 v[18:19], v[114:115], s[28:29] op_sel_hi:[1,0]
	v_add_f32_e32 v30, 1.0, v32
	v_rcp_f32_e32 v11, v11
	s_nop 0
	v_mul_f32_e32 v11, v14, v11
	v_mul_f32_e32 v28, 0xbfb8aa3b, v12
	v_exp_f32_e32 v28, v28
	v_mul_f32_e32 v11, v22, v11
	v_add_f32_e32 v28, 1.0, v28
	v_rcp_f32_e32 v14, v30
	s_nop 0
	v_mul_f32_e32 v14, v15, v14
	v_mul_f32_e32 v14, v23, v14
	v_mul_f32_e32 v23, 0xbfb8aa3b, v13
	v_exp_f32_e32 v23, v23
	s_nop 0
	v_add_f32_e32 v23, 1.0, v23
	v_rcp_f32_e32 v15, v28
	s_nop 0
	v_mul_f32_e32 v12, v12, v15
	v_mul_f32_e32 v15, v20, v12
	v_rcp_f32_e32 v12, v23
	s_nop 0
	v_mul_f32_e32 v12, v13, v12
	v_mul_f32_e32 v13, v21, v12
	v_mul_f32_e32 v12, 0xbfb8aa3b, v18
	v_exp_f32_e32 v20, v12
	v_med3_f32 v11, v11, s75, v239
	v_med3_f32 v14, v14, s75, v239
	v_mov_b32_e32 v12, v203
	v_cvt_pk_fp8_f32 v12, v11, v14
	v_add_f32_e32 v11, 1.0, v20
	v_med3_f32 v15, v15, s75, v239
	v_med3_f32 v13, v13, s75, v239
	v_cvt_pk_fp8_f32 v12, v15, v13 op_sel:[0,0,1]
	v_mul_f32_e32 v21, 0xbfb8aa3b, v19
	v_exp_f32_e32 v21, v21
	s_nop 0
	v_add_f32_e32 v14, 1.0, v21
	v_pk_mul_f32 v[16:17], v[116:117], s[28:29] op_sel_hi:[1,0]
	v_rcp_f32_e32 v11, v11
	s_nop 0
	v_mul_f32_e32 v11, v18, v11
	v_mul_f32_e32 v18, 0xbfb8aa3b, v16
	v_exp_f32_e32 v18, v18
	s_nop 0
	v_add_f32_e32 v18, 1.0, v18
	v_rcp_f32_e32 v13, v14
	s_nop 0
	v_mul_f32_e32 v13, v19, v13
	v_mul_f32_e32 v19, 0xbfb8aa3b, v17
	v_exp_f32_e32 v19, v19
	s_nop 0
	v_add_f32_e32 v19, 1.0, v19
	v_rcp_f32_e32 v14, v18
	s_nop 0
	v_mul_f32_e32 v14, v16, v14
	v_pk_mul_f32 v[26:27], v[82:83], s[30:31] op_sel_hi:[1,0]
	v_mul_f32_e32 v11, v26, v11
	v_mul_f32_e32 v13, v27, v13
	v_med3_f32 v11, v11, s75, v239
	v_med3_f32 v16, v13, s75, v239
	v_mov_b32_e32 v13, v203
	v_cvt_pk_fp8_f32 v13, v11, v16
	v_pk_mul_f32 v[24:25], v[84:85], s[30:31] op_sel_hi:[1,0]
	v_rcp_f32_e32 v15, v19
	s_nop 0
	v_mul_f32_e32 v15, v17, v15
	ds_read_b128 v[2:5], v9 offset:1024
	v_mul_f32_e32 v14, v24, v14
	v_mul_f32_e32 v11, v25, v15
	v_med3_f32 v14, v14, s75, v239
	v_med3_f32 v11, v11, s75, v239
	v_cvt_pk_fp8_f32 v13, v14, v11 op_sel:[0,0,1]
	v_add_u32_e32 v11, 0x4000, v10
	s_waitcnt lgkmcnt(0)
	global_store_dwordx4 v11, v[2:5], s[16:17] sc1
	ds_write_b64 v8, v[6:7]
	ds_write_b64 v8, v[12:13] offset:512
	v_pk_mul_f32 v[12:13], v[110:111], s[28:29] op_sel_hi:[1,0]
	v_pk_mul_f32 v[6:7], v[112:113], s[28:29] op_sel_hi:[1,0]
	v_mul_f32_e32 v11, 0xbfb8aa3b, v12
	v_exp_f32_e32 v11, v11
	v_mul_f32_e32 v30, 0xbfb8aa3b, v13
	v_exp_f32_e32 v30, v30
	v_pk_mul_f32 v[20:21], v[78:79], s[30:31] op_sel_hi:[1,0]
	v_add_f32_e32 v11, 1.0, v11
	v_pk_mul_f32 v[18:19], v[80:81], s[30:31] op_sel_hi:[1,0]
	v_pk_mul_f32 v[16:17], v[106:107], s[28:29] op_sel_hi:[1,0]
	v_pk_mul_f32 v[14:15], v[108:109], s[28:29] op_sel_hi:[1,0]
	v_add_f32_e32 v28, 1.0, v30
	v_rcp_f32_e32 v11, v11
	s_nop 0
	v_mul_f32_e32 v11, v12, v11
	v_mul_f32_e32 v26, 0xbfb8aa3b, v6
	v_exp_f32_e32 v26, v26
	v_mul_f32_e32 v11, v20, v11
	v_add_f32_e32 v26, 1.0, v26
	v_rcp_f32_e32 v12, v28
	s_nop 0
	v_mul_f32_e32 v12, v13, v12
	v_mul_f32_e32 v12, v21, v12
	v_mul_f32_e32 v21, 0xbfb8aa3b, v7
	v_exp_f32_e32 v21, v21
	s_nop 0
	v_add_f32_e32 v21, 1.0, v21
	v_rcp_f32_e32 v13, v26
	s_nop 0
	v_mul_f32_e32 v6, v6, v13
	v_mul_f32_e32 v13, v18, v6
	v_rcp_f32_e32 v6, v21
	s_nop 0
	v_mul_f32_e32 v6, v7, v6
	v_mul_f32_e32 v7, v19, v6
	v_mul_f32_e32 v6, 0xbfb8aa3b, v16
	v_exp_f32_e32 v18, v6
	v_med3_f32 v11, v11, s75, v239
	v_med3_f32 v12, v12, s75, v239
	v_mov_b32_e32 v6, v203
	v_cvt_pk_fp8_f32 v6, v11, v12
	v_add_f32_e32 v11, 1.0, v18
	v_med3_f32 v13, v13, s75, v239
	v_med3_f32 v7, v7, s75, v239
	v_cvt_pk_fp8_f32 v6, v13, v7 op_sel:[0,0,1]
	v_mul_f32_e32 v19, 0xbfb8aa3b, v17
	v_exp_f32_e32 v19, v19
	s_nop 0
	v_add_f32_e32 v12, 1.0, v19
	v_rcp_f32_e32 v7, v11
	s_nop 0
	v_mul_f32_e32 v7, v16, v7
	v_mul_f32_e32 v16, 0xbfb8aa3b, v14
	v_exp_f32_e32 v16, v16
	s_nop 0
	v_add_f32_e32 v16, 1.0, v16
	v_rcp_f32_e32 v11, v12
	s_nop 0
	v_mul_f32_e32 v11, v17, v11
	v_mul_f32_e32 v17, 0xbfb8aa3b, v15
	v_exp_f32_e32 v17, v17
	s_nop 0
	v_add_f32_e32 v17, 1.0, v17
	v_rcp_f32_e32 v12, v16
	s_nop 0
	v_mul_f32_e32 v12, v14, v12
	v_pk_mul_f32 v[24:25], v[74:75], s[30:31] op_sel_hi:[1,0]
	v_mul_f32_e32 v7, v24, v7
	v_mul_f32_e32 v11, v25, v11
	v_med3_f32 v14, v7, s75, v239
	v_med3_f32 v11, v11, s75, v239
	v_mov_b32_e32 v7, v203
	v_cvt_pk_fp8_f32 v7, v14, v11
	v_pk_mul_f32 v[22:23], v[76:77], s[30:31] op_sel_hi:[1,0]
	v_rcp_f32_e32 v13, v17
	s_nop 0
	v_mul_f32_e32 v13, v15, v13
	v_mul_f32_e32 v12, v22, v12
	v_mul_f32_e32 v11, v23, v13
	v_med3_f32 v12, v12, s75, v239
	v_med3_f32 v11, v11, s75, v239
	v_pk_mul_f32 v[14:15], v[102:103], s[28:29] op_sel_hi:[1,0]
	v_cvt_pk_fp8_f32 v7, v12, v11 op_sel:[0,0,1]
	v_mul_f32_e32 v11, 0xbfb8aa3b, v14
	v_exp_f32_e32 v11, v11
	v_mul_f32_e32 v32, 0xbfb8aa3b, v15
	v_exp_f32_e32 v32, v32
	v_pk_mul_f32 v[12:13], v[104:105], s[28:29] op_sel_hi:[1,0]
	v_add_f32_e32 v11, 1.0, v11
	v_pk_mul_f32 v[22:23], v[70:71], s[30:31] op_sel_hi:[1,0]
	v_pk_mul_f32 v[20:21], v[72:73], s[30:31] op_sel_hi:[1,0]
	v_pk_mul_f32 v[18:19], v[98:99], s[28:29] op_sel_hi:[1,0]
	v_add_f32_e32 v30, 1.0, v32
	v_rcp_f32_e32 v11, v11
	s_nop 0
	v_mul_f32_e32 v11, v14, v11
	v_mul_f32_e32 v28, 0xbfb8aa3b, v12
	v_exp_f32_e32 v28, v28
	v_mul_f32_e32 v11, v22, v11
	v_add_f32_e32 v28, 1.0, v28
	v_rcp_f32_e32 v14, v30
	s_nop 0
	v_mul_f32_e32 v14, v15, v14
	v_mul_f32_e32 v14, v23, v14
	v_mul_f32_e32 v23, 0xbfb8aa3b, v13
	v_exp_f32_e32 v23, v23
	s_nop 0
	v_add_f32_e32 v23, 1.0, v23
	v_rcp_f32_e32 v15, v28
	s_nop 0
	v_mul_f32_e32 v12, v12, v15
	v_mul_f32_e32 v15, v20, v12
	v_rcp_f32_e32 v12, v23
	s_nop 0
	v_mul_f32_e32 v12, v13, v12
	v_mul_f32_e32 v13, v21, v12
	v_mul_f32_e32 v12, 0xbfb8aa3b, v18
	v_exp_f32_e32 v20, v12
	v_med3_f32 v11, v11, s75, v239
	v_med3_f32 v14, v14, s75, v239
	v_mov_b32_e32 v12, v203
	v_cvt_pk_fp8_f32 v12, v11, v14
	v_add_f32_e32 v11, 1.0, v20
	v_med3_f32 v15, v15, s75, v239
	v_med3_f32 v13, v13, s75, v239
	v_cvt_pk_fp8_f32 v12, v15, v13 op_sel:[0,0,1]
	v_mul_f32_e32 v21, 0xbfb8aa3b, v19
	v_exp_f32_e32 v21, v21
	s_nop 0
	v_add_f32_e32 v14, 1.0, v21
	v_pk_mul_f32 v[16:17], v[100:101], s[28:29] op_sel_hi:[1,0]
	v_rcp_f32_e32 v11, v11
	s_nop 0
	v_mul_f32_e32 v11, v18, v11
	v_mul_f32_e32 v18, 0xbfb8aa3b, v16
	v_exp_f32_e32 v18, v18
	s_nop 0
	v_add_f32_e32 v18, 1.0, v18
	v_rcp_f32_e32 v13, v14
	s_nop 0
	v_mul_f32_e32 v13, v19, v13
	v_mul_f32_e32 v19, 0xbfb8aa3b, v17
	v_exp_f32_e32 v19, v19
	s_nop 0
	v_add_f32_e32 v19, 1.0, v19
	v_rcp_f32_e32 v14, v18
	s_nop 0
	v_mul_f32_e32 v14, v16, v14
	v_pk_mul_f32 v[26:27], v[66:67], s[30:31] op_sel_hi:[1,0]
	v_mul_f32_e32 v11, v26, v11
	v_mul_f32_e32 v13, v27, v13
	v_med3_f32 v11, v11, s75, v239
	v_med3_f32 v16, v13, s75, v239
	v_mov_b32_e32 v13, v203
	v_cvt_pk_fp8_f32 v13, v11, v16
	v_pk_mul_f32 v[24:25], v[68:69], s[30:31] op_sel_hi:[1,0]
	v_rcp_f32_e32 v15, v19
	s_nop 0
	v_mul_f32_e32 v15, v17, v15
	ds_read_b128 v[2:5], v9
	v_mul_f32_e32 v14, v24, v14
	v_mul_f32_e32 v11, v25, v15
	v_med3_f32 v14, v14, s75, v239
	v_med3_f32 v11, v11, s75, v239
	v_cvt_pk_fp8_f32 v13, v14, v11 op_sel:[0,0,1]
	v_add_u32_e32 v11, 0x10000, v10
	s_waitcnt lgkmcnt(0)
	global_store_dwordx4 v11, v[2:5], s[16:17] sc1
	ds_write_b64 v8, v[6:7] offset:1024
	ds_write_b64 v8, v[12:13] offset:1536
	ds_read_b128 v[2:5], v9 offset:1024
	v_add_u32_e32 v6, 0x14000, v10
	s_andn2_b64 vcc, exec, s[42:43]
	s_waitcnt lgkmcnt(0)
	global_store_dwordx4 v6, v[2:5], s[16:17] sc1
	s_cbranch_vccnz .LBB0_1680
	s_andn2_b64 vcc, exec, s[20:21]
	s_cbranch_vccnz .LBB0_1647
	s_barrier
	s_branch .LBB0_1647

.LBB0_1853:
	v_mov_b32_e32 v2, v232
	s_add_u32 s0, s79, 0xffffff00
	s_nop 15
	s_nop 15
	s_nop 15
	s_addc_u32 s1, s80, -1
	v_lshlrev_b32_e32 v3, 5, v2
	v_ashrrev_i32_e32 v4, 1, v2
	v_and_b32_e32 v3, 0x1e0, v3
	v_and_b32_e32 v5, -8, v4
	s_add_i32 s2, s33, s69
	v_add3_u32 v8, s53, v3, v5
	v_add_u32_e32 v10, s2, v4
	v_pk_mul_f32 v[4:5], v[190:191], s[28:29] op_sel_hi:[1,0]
	v_lshlrev_b32_e32 v2, 4, v2
	v_mul_f32_e32 v6, 0xbfb8aa3b, v4
	v_exp_f32_e32 v16, v6
	v_mul_f32_e32 v27, 0xbfb8aa3b, v5
	v_exp_f32_e32 v27, v27
	v_add_u32_e32 v9, s53, v2
	v_add_f32_e32 v22, 1.0, v16
	v_and_b32_e32 v11, 16, v2
	v_pk_mul_f32 v[2:3], v[192:193], s[28:29] op_sel_hi:[1,0]
	v_pk_mul_f32 v[16:17], v[158:159], s[30:31] op_sel_hi:[1,0]
	v_add_f32_e32 v25, 1.0, v27
	v_rcp_f32_e32 v23, v22
	s_nop 0
	v_mul_f32_e32 v4, v4, v23
	v_mul_f32_e32 v23, 0xbfb8aa3b, v2
	v_exp_f32_e32 v23, v23
	v_mul_f32_e32 v4, v4, v16
	v_add_f32_e32 v23, 1.0, v23
	v_mul_f32_e32 v22, 0xbfb8aa3b, v3
	v_rcp_f32_e32 v16, v25
	s_nop 0
	v_mul_f32_e32 v5, v5, v16
	v_exp_f32_e32 v22, v22
	v_mul_f32_e32 v5, v5, v17
	v_add_f32_e32 v22, 1.0, v22
	v_pk_mul_f32 v[14:15], v[160:161], s[30:31] op_sel_hi:[1,0]
	v_rcp_f32_e32 v16, v23
	s_nop 0
	v_mul_f32_e32 v2, v2, v16
	v_mul_f32_e32 v14, v2, v14
	v_pk_mul_f32 v[12:13], v[186:187], s[28:29] op_sel_hi:[1,0]
	v_rcp_f32_e32 v2, v22
	s_nop 0
	v_mul_f32_e32 v2, v3, v2
	v_mul_f32_e32 v3, v2, v15
	v_mul_f32_e32 v2, 0xbfb8aa3b, v12
	v_exp_f32_e32 v15, v2
	v_med3_f32 v4, v4, s75, v233
	v_med3_f32 v5, v5, s75, v233
	v_mov_b32_e32 v2, v203
	v_cvt_pk_fp8_f32 v2, v4, v5
	v_add_f32_e32 v4, 1.0, v15
	v_med3_f32 v14, v14, s75, v233
	v_med3_f32 v3, v3, s75, v233
	v_cvt_pk_fp8_f32 v2, v14, v3 op_sel:[0,0,1]
	v_mul_f32_e32 v16, 0xbfb8aa3b, v13
	v_exp_f32_e32 v16, v16
	s_nop 0
	v_add_f32_e32 v5, 1.0, v16
	v_pk_mul_f32 v[6:7], v[188:189], s[28:29] op_sel_hi:[1,0]
	v_mul_f32_e32 v14, 0xbfb8aa3b, v6
	v_exp_f32_e32 v14, v14
	v_rcp_f32_e32 v3, v4
	s_nop 0
	v_mul_f32_e32 v3, v12, v3
	v_add_f32_e32 v14, 1.0, v14
	v_rcp_f32_e32 v4, v5
	s_nop 0
	v_mul_f32_e32 v4, v13, v4
	v_mul_f32_e32 v13, 0xbfb8aa3b, v7
	v_exp_f32_e32 v13, v13
	s_nop 0
	v_add_f32_e32 v13, 1.0, v13
	v_rcp_f32_e32 v5, v14
	s_nop 0
	v_mul_f32_e32 v5, v6, v5
	v_pk_mul_f32 v[20:21], v[154:155], s[30:31] op_sel_hi:[1,0]
	v_mul_f32_e32 v3, v3, v20
	v_mul_f32_e32 v4, v4, v21
	v_pk_mul_f32 v[18:19], v[156:157], s[30:31] op_sel_hi:[1,0]
	v_rcp_f32_e32 v6, v13
	s_nop 0
	v_mul_f32_e32 v6, v7, v6
	v_med3_f32 v7, v3, s75, v233
	v_med3_f32 v4, v4, s75, v233
	v_mov_b32_e32 v3, v203
	v_cvt_pk_fp8_f32 v3, v7, v4
	v_mul_f32_e32 v4, v6, v19
	v_pk_mul_f32 v[6:7], v[182:183], s[28:29] op_sel_hi:[1,0]
	v_mul_f32_e32 v5, v5, v18
	v_mul_f32_e32 v12, 0xbfb8aa3b, v6
	v_exp_f32_e32 v18, v12
	v_mul_f32_e32 v29, 0xbfb8aa3b, v7
	v_exp_f32_e32 v29, v29
	v_med3_f32 v5, v5, s75, v233
	v_add_f32_e32 v24, 1.0, v18
	v_med3_f32 v4, v4, s75, v233
	v_cvt_pk_fp8_f32 v3, v5, v4 op_sel:[0,0,1]
	v_pk_mul_f32 v[4:5], v[184:185], s[28:29] op_sel_hi:[1,0]
	v_add_f32_e32 v27, 1.0, v29
	v_rcp_f32_e32 v25, v24
	s_nop 0
	v_mul_f32_e32 v6, v6, v25
	v_mul_f32_e32 v25, 0xbfb8aa3b, v4
	v_pk_mul_f32 v[18:19], v[150:151], s[30:31] op_sel_hi:[1,0]
	v_exp_f32_e32 v25, v25
	v_mul_f32_e32 v6, v6, v18
	v_add_f32_e32 v25, 1.0, v25
	v_mul_f32_e32 v24, 0xbfb8aa3b, v5
	v_rcp_f32_e32 v18, v27
	s_nop 0
	v_mul_f32_e32 v7, v7, v18
	v_exp_f32_e32 v24, v24
	v_mul_f32_e32 v7, v7, v19
	v_add_f32_e32 v24, 1.0, v24
	v_pk_mul_f32 v[16:17], v[152:153], s[30:31] op_sel_hi:[1,0]
	v_rcp_f32_e32 v18, v25
	s_nop 0
	v_mul_f32_e32 v4, v4, v18
	v_mul_f32_e32 v16, v4, v16
	v_pk_mul_f32 v[14:15], v[178:179], s[28:29] op_sel_hi:[1,0]
	v_rcp_f32_e32 v4, v24
	s_nop 0
	v_mul_f32_e32 v4, v5, v4
	v_mul_f32_e32 v5, v4, v17
	v_mul_f32_e32 v4, 0xbfb8aa3b, v14
	v_exp_f32_e32 v17, v4
	v_med3_f32 v6, v6, s75, v233
	v_med3_f32 v7, v7, s75, v233
	v_mov_b32_e32 v4, v203
	v_cvt_pk_fp8_f32 v4, v6, v7
	v_add_f32_e32 v6, 1.0, v17
	v_med3_f32 v16, v16, s75, v233
	v_med3_f32 v5, v5, s75, v233
	v_cvt_pk_fp8_f32 v4, v16, v5 op_sel:[0,0,1]
	v_mul_f32_e32 v18, 0xbfb8aa3b, v15
	v_exp_f32_e32 v18, v18
	s_nop 0
	v_add_f32_e32 v7, 1.0, v18
	v_pk_mul_f32 v[12:13], v[180:181], s[28:29] op_sel_hi:[1,0]
	v_mul_f32_e32 v16, 0xbfb8aa3b, v12
	v_exp_f32_e32 v16, v16
	v_rcp_f32_e32 v5, v6
	s_nop 0
	v_mul_f32_e32 v5, v14, v5
	v_add_f32_e32 v16, 1.0, v16
	v_rcp_f32_e32 v6, v7
	s_nop 0
	v_mul_f32_e32 v6, v15, v6
	v_mul_f32_e32 v15, 0xbfb8aa3b, v13
	v_exp_f32_e32 v15, v15
	s_nop 0
	v_add_f32_e32 v15, 1.0, v15
	v_rcp_f32_e32 v7, v16
	s_nop 0
	v_mul_f32_e32 v7, v12, v7
	v_pk_mul_f32 v[22:23], v[146:147], s[30:31] op_sel_hi:[1,0]
	v_mul_f32_e32 v5, v5, v22
	v_mul_f32_e32 v6, v6, v23
	v_pk_mul_f32 v[20:21], v[148:149], s[30:31] op_sel_hi:[1,0]
	v_rcp_f32_e32 v12, v15
	s_nop 0
	v_mul_f32_e32 v12, v13, v12
	v_med3_f32 v13, v5, s75, v233
	v_med3_f32 v6, v6, s75, v233
	v_mov_b32_e32 v5, v203
	v_cvt_pk_fp8_f32 v5, v13, v6
	v_mul_f32_e32 v6, v12, v21
	v_pk_mul_f32 v[12:13], v[174:175], s[28:29] op_sel_hi:[1,0]
	v_mul_f32_e32 v7, v7, v20
	v_mul_f32_e32 v14, 0xbfb8aa3b, v12
	v_exp_f32_e32 v20, v14
	v_mul_f32_e32 v31, 0xbfb8aa3b, v13
	v_exp_f32_e32 v31, v31
	v_med3_f32 v7, v7, s75, v233
	v_add_f32_e32 v26, 1.0, v20
	v_med3_f32 v6, v6, s75, v233
	v_cvt_pk_fp8_f32 v5, v7, v6 op_sel:[0,0,1]
	v_lshl_or_b32 v6, s18, 7, v11
	v_add_f32_e32 v29, 1.0, v31
	v_or_b32_e32 v11, s70, v6
	v_pk_mul_f32 v[6:7], v[176:177], s[28:29] op_sel_hi:[1,0]
	v_rcp_f32_e32 v27, v26
	s_nop 0
	v_mul_f32_e32 v12, v12, v27
	v_mul_f32_e32 v27, 0xbfb8aa3b, v6
	v_pk_mul_f32 v[20:21], v[142:143], s[30:31] op_sel_hi:[1,0]
	v_exp_f32_e32 v27, v27
	v_mul_f32_e32 v12, v12, v20
	v_add_f32_e32 v27, 1.0, v27
	v_mul_f32_e32 v26, 0xbfb8aa3b, v7
	v_rcp_f32_e32 v20, v29
	s_nop 0
	v_mul_f32_e32 v13, v13, v20
	v_exp_f32_e32 v26, v26
	v_mul_f32_e32 v13, v13, v21
	v_add_f32_e32 v26, 1.0, v26
	v_pk_mul_f32 v[18:19], v[144:145], s[30:31] op_sel_hi:[1,0]
	v_rcp_f32_e32 v20, v27
	s_nop 0
	v_mul_f32_e32 v6, v6, v20
	v_mul_f32_e32 v18, v6, v18
	v_pk_mul_f32 v[16:17], v[170:171], s[28:29] op_sel_hi:[1,0]
	v_rcp_f32_e32 v6, v26
	s_nop 0
	v_mul_f32_e32 v6, v7, v6
	v_mul_f32_e32 v7, v6, v19
	v_mul_f32_e32 v6, 0xbfb8aa3b, v16
	v_exp_f32_e32 v19, v6
	v_med3_f32 v12, v12, s75, v233
	v_med3_f32 v13, v13, s75, v233
	v_mov_b32_e32 v6, v203
	v_cvt_pk_fp8_f32 v6, v12, v13
	v_add_f32_e32 v12, 1.0, v19
	v_med3_f32 v18, v18, s75, v233
	v_med3_f32 v7, v7, s75, v233
	v_cvt_pk_fp8_f32 v6, v18, v7 op_sel:[0,0,1]
	v_mul_f32_e32 v20, 0xbfb8aa3b, v17
	v_exp_f32_e32 v20, v20
	s_nop 0
	v_add_f32_e32 v13, 1.0, v20
	v_pk_mul_f32 v[14:15], v[172:173], s[28:29] op_sel_hi:[1,0]
	v_mul_f32_e32 v18, 0xbfb8aa3b, v14
	v_exp_f32_e32 v18, v18
	v_rcp_f32_e32 v7, v12
	s_nop 0
	v_mul_f32_e32 v7, v16, v7
	v_add_f32_e32 v18, 1.0, v18
	v_rcp_f32_e32 v12, v13
	s_nop 0
	v_mul_f32_e32 v12, v17, v12
	v_mul_f32_e32 v17, 0xbfb8aa3b, v15
	v_exp_f32_e32 v17, v17
	s_nop 0
	v_add_f32_e32 v17, 1.0, v17
	v_rcp_f32_e32 v13, v18
	s_nop 0
	v_mul_f32_e32 v13, v14, v13
	v_pk_mul_f32 v[24:25], v[138:139], s[30:31] op_sel_hi:[1,0]
	v_mul_f32_e32 v7, v7, v24
	v_mul_f32_e32 v12, v12, v25
	v_pk_mul_f32 v[22:23], v[140:141], s[30:31] op_sel_hi:[1,0]
	v_rcp_f32_e32 v14, v17
	s_nop 0
	v_mul_f32_e32 v14, v15, v14
	v_med3_f32 v15, v7, s75, v233
	v_med3_f32 v12, v12, s75, v233
	v_mov_b32_e32 v7, v203
	v_cvt_pk_fp8_f32 v7, v15, v12
	v_mul_f32_e32 v12, v14, v23
	v_pk_mul_f32 v[14:15], v[166:167], s[28:29] op_sel_hi:[1,0]
	v_mul_f32_e32 v13, v13, v22
	v_mul_f32_e32 v16, 0xbfb8aa3b, v14
	v_exp_f32_e32 v22, v16
	v_mul_f32_e32 v33, 0xbfb8aa3b, v15
	v_exp_f32_e32 v33, v33
	v_med3_f32 v13, v13, s75, v233
	v_add_f32_e32 v28, 1.0, v22
	v_med3_f32 v12, v12, s75, v233
	v_cvt_pk_fp8_f32 v7, v13, v12 op_sel:[0,0,1]
	v_pk_mul_f32 v[12:13], v[168:169], s[28:29] op_sel_hi:[1,0]
	s_waitcnt lgkmcnt(0)
	v_add_f32_e32 v31, 1.0, v33
	v_rcp_f32_e32 v29, v28
	s_nop 0
	v_mul_f32_e32 v14, v14, v29
	v_mul_f32_e32 v29, 0xbfb8aa3b, v12
	v_pk_mul_f32 v[22:23], v[134:135], s[30:31] op_sel_hi:[1,0]
	v_exp_f32_e32 v29, v29
	v_mul_f32_e32 v14, v14, v22
	v_add_f32_e32 v29, 1.0, v29
	v_mul_f32_e32 v28, 0xbfb8aa3b, v13
	v_rcp_f32_e32 v22, v31
	s_nop 0
	v_mul_f32_e32 v15, v15, v22
	v_exp_f32_e32 v28, v28
	v_mul_f32_e32 v15, v15, v23
	v_add_f32_e32 v28, 1.0, v28
	v_pk_mul_f32 v[20:21], v[136:137], s[30:31] op_sel_hi:[1,0]
	v_rcp_f32_e32 v22, v29
	s_nop 0
	v_mul_f32_e32 v12, v12, v22
	v_mul_f32_e32 v20, v12, v20
	v_pk_mul_f32 v[18:19], v[162:163], s[28:29] op_sel_hi:[1,0]
	v_rcp_f32_e32 v12, v28
	s_nop 0
	v_mul_f32_e32 v12, v13, v12
	v_mul_f32_e32 v13, v12, v21
	v_mul_f32_e32 v12, 0xbfb8aa3b, v18
	v_exp_f32_e32 v21, v12
	v_med3_f32 v14, v14, s75, v233
	v_med3_f32 v15, v15, s75, v233
	v_mov_b32_e32 v12, v203
	v_cvt_pk_fp8_f32 v12, v14, v15
	v_add_f32_e32 v14, 1.0, v21
	v_med3_f32 v20, v20, s75, v233
	v_med3_f32 v13, v13, s75, v233
	v_cvt_pk_fp8_f32 v12, v20, v13 op_sel:[0,0,1]
	v_mul_f32_e32 v22, 0xbfb8aa3b, v19
	v_exp_f32_e32 v22, v22
	s_nop 0
	v_add_f32_e32 v15, 1.0, v22
	v_pk_mul_f32 v[16:17], v[164:165], s[28:29] op_sel_hi:[1,0]
	v_mul_f32_e32 v20, 0xbfb8aa3b, v16
	v_exp_f32_e32 v20, v20
	v_rcp_f32_e32 v13, v14
	s_nop 0
	v_mul_f32_e32 v13, v18, v13
	v_add_f32_e32 v20, 1.0, v20
	v_rcp_f32_e32 v14, v15
	s_nop 0
	v_mul_f32_e32 v14, v19, v14
	v_mul_f32_e32 v19, 0xbfb8aa3b, v17
	v_exp_f32_e32 v19, v19
	s_nop 0
	v_add_f32_e32 v19, 1.0, v19
	v_rcp_f32_e32 v15, v20
	s_nop 0
	v_mul_f32_e32 v15, v16, v15
	v_pk_mul_f32 v[26:27], v[130:131], s[30:31] op_sel_hi:[1,0]
	v_mul_f32_e32 v13, v13, v26
	v_mul_f32_e32 v14, v14, v27
	v_rcp_f32_e32 v16, v19
	s_nop 0
	v_mul_f32_e32 v16, v17, v16
	v_med3_f32 v17, v13, s75, v233
	v_med3_f32 v14, v14, s75, v233
	v_mov_b32_e32 v13, v203
	v_cvt_pk_fp8_f32 v13, v17, v14
	ds_write_b64 v8, v[2:3]
	ds_write_b64 v8, v[4:5] offset:512
	v_pk_mul_f32 v[24:25], v[132:133], s[30:31] op_sel_hi:[1,0]
	ds_read_b128 v[2:5], v9
	v_mul_f32_e32 v15, v15, v24
	v_mul_f32_e32 v14, v16, v25
	v_med3_f32 v15, v15, s75, v233
	v_med3_f32 v14, v14, s75, v233
	v_cvt_pk_fp8_f32 v13, v15, v14 op_sel:[0,0,1]
	v_lshl_add_u32 v10, v10, 9, v11
	s_waitcnt lgkmcnt(0)
	global_store_dwordx4 v10, v[2:5], s[16:17] sc1
	ds_write_b64 v8, v[6:7] offset:1024
	ds_write_b64 v8, v[12:13] offset:1536
	v_pk_mul_f32 v[12:13], v[126:127], s[28:29] op_sel_hi:[1,0]
	v_pk_mul_f32 v[6:7], v[128:129], s[28:29] op_sel_hi:[1,0]
	v_mul_f32_e32 v11, 0xbfb8aa3b, v12
	v_exp_f32_e32 v11, v11
	v_mul_f32_e32 v30, 0xbfb8aa3b, v13
	v_exp_f32_e32 v30, v30
	v_pk_mul_f32 v[20:21], v[94:95], s[30:31] op_sel_hi:[1,0]
	v_add_f32_e32 v11, 1.0, v11
	v_pk_mul_f32 v[18:19], v[96:97], s[30:31] op_sel_hi:[1,0]
	v_pk_mul_f32 v[16:17], v[122:123], s[28:29] op_sel_hi:[1,0]
	v_pk_mul_f32 v[14:15], v[124:125], s[28:29] op_sel_hi:[1,0]
	v_add_f32_e32 v28, 1.0, v30
	v_rcp_f32_e32 v11, v11
	s_nop 0
	v_mul_f32_e32 v11, v12, v11
	v_mul_f32_e32 v26, 0xbfb8aa3b, v6
	v_exp_f32_e32 v26, v26
	v_mul_f32_e32 v11, v20, v11
	v_add_f32_e32 v26, 1.0, v26
	v_rcp_f32_e32 v12, v28
	s_nop 0
	v_mul_f32_e32 v12, v13, v12
	v_mul_f32_e32 v12, v21, v12
	v_mul_f32_e32 v21, 0xbfb8aa3b, v7
	v_exp_f32_e32 v21, v21
	s_nop 0
	v_add_f32_e32 v21, 1.0, v21
	v_rcp_f32_e32 v13, v26
	s_nop 0
	v_mul_f32_e32 v6, v6, v13
	v_mul_f32_e32 v13, v18, v6
	v_rcp_f32_e32 v6, v21
	s_nop 0
	v_mul_f32_e32 v6, v7, v6
	v_mul_f32_e32 v7, v19, v6
	v_mul_f32_e32 v6, 0xbfb8aa3b, v16
	v_exp_f32_e32 v18, v6
	v_med3_f32 v11, v11, s75, v233
	v_med3_f32 v12, v12, s75, v233
	v_mov_b32_e32 v6, v203
	v_cvt_pk_fp8_f32 v6, v11, v12
	v_add_f32_e32 v11, 1.0, v18
	v_med3_f32 v13, v13, s75, v233
	v_med3_f32 v7, v7, s75, v233
	v_cvt_pk_fp8_f32 v6, v13, v7 op_sel:[0,0,1]
	v_mul_f32_e32 v19, 0xbfb8aa3b, v17
	v_exp_f32_e32 v19, v19
	s_nop 0
	v_add_f32_e32 v12, 1.0, v19
	v_rcp_f32_e32 v7, v11
	s_nop 0
	v_mul_f32_e32 v7, v16, v7
	v_mul_f32_e32 v16, 0xbfb8aa3b, v14
	v_exp_f32_e32 v16, v16
	s_nop 0
	v_add_f32_e32 v16, 1.0, v16
	v_rcp_f32_e32 v11, v12
	s_nop 0
	v_mul_f32_e32 v11, v17, v11
	v_mul_f32_e32 v17, 0xbfb8aa3b, v15
	v_exp_f32_e32 v17, v17
	s_nop 0
	v_add_f32_e32 v17, 1.0, v17
	v_rcp_f32_e32 v12, v16
	s_nop 0
	v_mul_f32_e32 v12, v14, v12
	v_pk_mul_f32 v[24:25], v[90:91], s[30:31] op_sel_hi:[1,0]
	v_mul_f32_e32 v7, v24, v7
	v_mul_f32_e32 v11, v25, v11
	v_med3_f32 v14, v7, s75, v233
	v_med3_f32 v11, v11, s75, v233
	v_mov_b32_e32 v7, v203
	v_cvt_pk_fp8_f32 v7, v14, v11
	v_pk_mul_f32 v[22:23], v[92:93], s[30:31] op_sel_hi:[1,0]
	v_rcp_f32_e32 v13, v17
	s_nop 0
	v_mul_f32_e32 v13, v15, v13
	v_mul_f32_e32 v12, v22, v12
	v_mul_f32_e32 v11, v23, v13
	v_med3_f32 v12, v12, s75, v233
	v_med3_f32 v11, v11, s75, v233
	v_pk_mul_f32 v[14:15], v[118:119], s[28:29] op_sel_hi:[1,0]
	v_cvt_pk_fp8_f32 v7, v12, v11 op_sel:[0,0,1]
	v_mul_f32_e32 v11, 0xbfb8aa3b, v14
	v_exp_f32_e32 v11, v11
	v_mul_f32_e32 v32, 0xbfb8aa3b, v15
	v_exp_f32_e32 v32, v32
	v_pk_mul_f32 v[12:13], v[120:121], s[28:29] op_sel_hi:[1,0]
	v_add_f32_e32 v11, 1.0, v11
	v_pk_mul_f32 v[22:23], v[86:87], s[30:31] op_sel_hi:[1,0]
	v_pk_mul_f32 v[20:21], v[88:89], s[30:31] op_sel_hi:[1,0]
	v_pk_mul_f32 v[18:19], v[114:115], s[28:29] op_sel_hi:[1,0]
	v_add_f32_e32 v30, 1.0, v32
	v_rcp_f32_e32 v11, v11
	s_nop 0
	v_mul_f32_e32 v11, v14, v11
	v_mul_f32_e32 v28, 0xbfb8aa3b, v12
	v_exp_f32_e32 v28, v28
	v_mul_f32_e32 v11, v22, v11
	v_add_f32_e32 v28, 1.0, v28
	v_rcp_f32_e32 v14, v30
	s_nop 0
	v_mul_f32_e32 v14, v15, v14
	v_mul_f32_e32 v14, v23, v14
	v_mul_f32_e32 v23, 0xbfb8aa3b, v13
	v_exp_f32_e32 v23, v23
	s_nop 0
	v_add_f32_e32 v23, 1.0, v23
	v_rcp_f32_e32 v15, v28
	s_nop 0
	v_mul_f32_e32 v12, v12, v15
	v_mul_f32_e32 v15, v20, v12
	v_rcp_f32_e32 v12, v23
	s_nop 0
	v_mul_f32_e32 v12, v13, v12
	v_mul_f32_e32 v13, v21, v12
	v_mul_f32_e32 v12, 0xbfb8aa3b, v18
	v_exp_f32_e32 v20, v12
	v_med3_f32 v11, v11, s75, v233
	v_med3_f32 v14, v14, s75, v233
	v_mov_b32_e32 v12, v203
	v_cvt_pk_fp8_f32 v12, v11, v14
	v_add_f32_e32 v11, 1.0, v20
	v_med3_f32 v15, v15, s75, v233
	v_med3_f32 v13, v13, s75, v233
	v_cvt_pk_fp8_f32 v12, v15, v13 op_sel:[0,0,1]
	v_mul_f32_e32 v21, 0xbfb8aa3b, v19
	v_exp_f32_e32 v21, v21
	s_nop 0
	v_add_f32_e32 v14, 1.0, v21
	v_pk_mul_f32 v[16:17], v[116:117], s[28:29] op_sel_hi:[1,0]
	v_rcp_f32_e32 v11, v11
	s_nop 0
	v_mul_f32_e32 v11, v18, v11
	v_mul_f32_e32 v18, 0xbfb8aa3b, v16
	v_exp_f32_e32 v18, v18
	s_nop 0
	v_add_f32_e32 v18, 1.0, v18
	v_rcp_f32_e32 v13, v14
	s_nop 0
	v_mul_f32_e32 v13, v19, v13
	v_mul_f32_e32 v19, 0xbfb8aa3b, v17
	v_exp_f32_e32 v19, v19
	s_nop 0
	v_add_f32_e32 v19, 1.0, v19
	v_rcp_f32_e32 v14, v18
	s_nop 0
	v_mul_f32_e32 v14, v16, v14
	v_pk_mul_f32 v[26:27], v[82:83], s[30:31] op_sel_hi:[1,0]
	v_mul_f32_e32 v11, v26, v11
	v_mul_f32_e32 v13, v27, v13
	v_med3_f32 v11, v11, s75, v233
	v_med3_f32 v16, v13, s75, v233
	v_mov_b32_e32 v13, v203
	v_cvt_pk_fp8_f32 v13, v11, v16
	v_pk_mul_f32 v[24:25], v[84:85], s[30:31] op_sel_hi:[1,0]
	v_rcp_f32_e32 v15, v19
	s_nop 0
	v_mul_f32_e32 v15, v17, v15
	ds_read_b128 v[2:5], v9 offset:1024
	v_mul_f32_e32 v14, v24, v14
	v_mul_f32_e32 v11, v25, v15
	v_med3_f32 v14, v14, s75, v233
	v_med3_f32 v11, v11, s75, v233
	v_cvt_pk_fp8_f32 v13, v14, v11 op_sel:[0,0,1]
	v_add_u32_e32 v11, 0x4000, v10
	s_waitcnt lgkmcnt(0)
	global_store_dwordx4 v11, v[2:5], s[16:17] sc1
	ds_write_b64 v8, v[6:7]
	ds_write_b64 v8, v[12:13] offset:512
	v_pk_mul_f32 v[12:13], v[110:111], s[28:29] op_sel_hi:[1,0]
	v_pk_mul_f32 v[6:7], v[112:113], s[28:29] op_sel_hi:[1,0]
	v_mul_f32_e32 v11, 0xbfb8aa3b, v12
	v_exp_f32_e32 v11, v11
	v_mul_f32_e32 v30, 0xbfb8aa3b, v13
	v_exp_f32_e32 v30, v30
	v_pk_mul_f32 v[20:21], v[78:79], s[30:31] op_sel_hi:[1,0]
	v_add_f32_e32 v11, 1.0, v11
	v_pk_mul_f32 v[18:19], v[80:81], s[30:31] op_sel_hi:[1,0]
	v_pk_mul_f32 v[16:17], v[106:107], s[28:29] op_sel_hi:[1,0]
	v_pk_mul_f32 v[14:15], v[108:109], s[28:29] op_sel_hi:[1,0]
	v_add_f32_e32 v28, 1.0, v30
	v_rcp_f32_e32 v11, v11
	s_nop 0
	v_mul_f32_e32 v11, v12, v11
	v_mul_f32_e32 v26, 0xbfb8aa3b, v6
	v_exp_f32_e32 v26, v26
	v_mul_f32_e32 v11, v20, v11
	v_add_f32_e32 v26, 1.0, v26
	v_rcp_f32_e32 v12, v28
	s_nop 0
	v_mul_f32_e32 v12, v13, v12
	v_mul_f32_e32 v12, v21, v12
	v_mul_f32_e32 v21, 0xbfb8aa3b, v7
	v_exp_f32_e32 v21, v21
	s_nop 0
	v_add_f32_e32 v21, 1.0, v21
	v_rcp_f32_e32 v13, v26
	s_nop 0
	v_mul_f32_e32 v6, v6, v13
	v_mul_f32_e32 v13, v18, v6
	v_rcp_f32_e32 v6, v21
	s_nop 0
	v_mul_f32_e32 v6, v7, v6
	v_mul_f32_e32 v7, v19, v6
	v_mul_f32_e32 v6, 0xbfb8aa3b, v16
	v_exp_f32_e32 v18, v6
	v_med3_f32 v11, v11, s75, v233
	v_med3_f32 v12, v12, s75, v233
	v_mov_b32_e32 v6, v203
	v_cvt_pk_fp8_f32 v6, v11, v12
	v_add_f32_e32 v11, 1.0, v18
	v_med3_f32 v13, v13, s75, v233
	v_med3_f32 v7, v7, s75, v233
	v_cvt_pk_fp8_f32 v6, v13, v7 op_sel:[0,0,1]
	v_mul_f32_e32 v19, 0xbfb8aa3b, v17
	v_exp_f32_e32 v19, v19
	s_nop 0
	v_add_f32_e32 v12, 1.0, v19
	v_rcp_f32_e32 v7, v11
	s_nop 0
	v_mul_f32_e32 v7, v16, v7
	v_mul_f32_e32 v16, 0xbfb8aa3b, v14
	v_exp_f32_e32 v16, v16
	s_nop 0
	v_add_f32_e32 v16, 1.0, v16
	v_rcp_f32_e32 v11, v12
	s_nop 0
	v_mul_f32_e32 v11, v17, v11
	v_mul_f32_e32 v17, 0xbfb8aa3b, v15
	v_exp_f32_e32 v17, v17
	s_nop 0
	v_add_f32_e32 v17, 1.0, v17
	v_rcp_f32_e32 v12, v16
	s_nop 0
	v_mul_f32_e32 v12, v14, v12
	v_pk_mul_f32 v[24:25], v[74:75], s[30:31] op_sel_hi:[1,0]
	v_mul_f32_e32 v7, v24, v7
	v_mul_f32_e32 v11, v25, v11
	v_med3_f32 v14, v7, s75, v233
	v_med3_f32 v11, v11, s75, v233
	v_mov_b32_e32 v7, v203
	v_cvt_pk_fp8_f32 v7, v14, v11
	v_pk_mul_f32 v[22:23], v[76:77], s[30:31] op_sel_hi:[1,0]
	v_rcp_f32_e32 v13, v17
	s_nop 0
	v_mul_f32_e32 v13, v15, v13
	v_mul_f32_e32 v12, v22, v12
	v_mul_f32_e32 v11, v23, v13
	v_med3_f32 v12, v12, s75, v233
	v_med3_f32 v11, v11, s75, v233
	v_pk_mul_f32 v[14:15], v[102:103], s[28:29] op_sel_hi:[1,0]
	v_cvt_pk_fp8_f32 v7, v12, v11 op_sel:[0,0,1]
	v_mul_f32_e32 v11, 0xbfb8aa3b, v14
	v_exp_f32_e32 v11, v11
	v_mul_f32_e32 v32, 0xbfb8aa3b, v15
	v_exp_f32_e32 v32, v32
	v_pk_mul_f32 v[12:13], v[104:105], s[28:29] op_sel_hi:[1,0]
	v_add_f32_e32 v11, 1.0, v11
	v_pk_mul_f32 v[22:23], v[70:71], s[30:31] op_sel_hi:[1,0]
	v_pk_mul_f32 v[20:21], v[72:73], s[30:31] op_sel_hi:[1,0]
	v_pk_mul_f32 v[18:19], v[98:99], s[28:29] op_sel_hi:[1,0]
	v_add_f32_e32 v30, 1.0, v32
	v_rcp_f32_e32 v11, v11
	s_nop 0
	v_mul_f32_e32 v11, v14, v11
	v_mul_f32_e32 v28, 0xbfb8aa3b, v12
	v_exp_f32_e32 v28, v28
	v_mul_f32_e32 v11, v22, v11
	v_add_f32_e32 v28, 1.0, v28
	v_rcp_f32_e32 v14, v30
	s_nop 0
	v_mul_f32_e32 v14, v15, v14
	v_mul_f32_e32 v14, v23, v14
	v_mul_f32_e32 v23, 0xbfb8aa3b, v13
	v_exp_f32_e32 v23, v23
	s_nop 0
	v_add_f32_e32 v23, 1.0, v23
	v_rcp_f32_e32 v15, v28
	s_nop 0
	v_mul_f32_e32 v12, v12, v15
	v_mul_f32_e32 v15, v20, v12
	v_rcp_f32_e32 v12, v23
	s_nop 0
	v_mul_f32_e32 v12, v13, v12
	v_mul_f32_e32 v13, v21, v12
	v_mul_f32_e32 v12, 0xbfb8aa3b, v18
	v_exp_f32_e32 v20, v12
	v_med3_f32 v11, v11, s75, v233
	v_med3_f32 v14, v14, s75, v233
	v_mov_b32_e32 v12, v203
	v_cvt_pk_fp8_f32 v12, v11, v14
	v_add_f32_e32 v11, 1.0, v20
	v_med3_f32 v15, v15, s75, v233
	v_med3_f32 v13, v13, s75, v233
	v_cvt_pk_fp8_f32 v12, v15, v13 op_sel:[0,0,1]
	v_mul_f32_e32 v21, 0xbfb8aa3b, v19
	v_exp_f32_e32 v21, v21
	s_nop 0
	v_add_f32_e32 v14, 1.0, v21
	v_pk_mul_f32 v[16:17], v[100:101], s[28:29] op_sel_hi:[1,0]
	v_rcp_f32_e32 v11, v11
	s_nop 0
	v_mul_f32_e32 v11, v18, v11
	v_mul_f32_e32 v18, 0xbfb8aa3b, v16
	v_exp_f32_e32 v18, v18
	s_nop 0
	v_add_f32_e32 v18, 1.0, v18
	v_rcp_f32_e32 v13, v14
	s_nop 0
	v_mul_f32_e32 v13, v19, v13
	v_mul_f32_e32 v19, 0xbfb8aa3b, v17
	v_exp_f32_e32 v19, v19
	s_nop 0
	v_add_f32_e32 v19, 1.0, v19
	v_rcp_f32_e32 v14, v18
	s_nop 0
	v_mul_f32_e32 v14, v16, v14
	v_pk_mul_f32 v[26:27], v[66:67], s[30:31] op_sel_hi:[1,0]
	v_mul_f32_e32 v11, v26, v11
	v_mul_f32_e32 v13, v27, v13
	v_med3_f32 v11, v11, s75, v233
	v_med3_f32 v16, v13, s75, v233
	v_mov_b32_e32 v13, v203
	v_cvt_pk_fp8_f32 v13, v11, v16
	v_pk_mul_f32 v[24:25], v[68:69], s[30:31] op_sel_hi:[1,0]
	v_rcp_f32_e32 v15, v19
	s_nop 0
	v_mul_f32_e32 v15, v17, v15
	ds_read_b128 v[2:5], v9
	v_mul_f32_e32 v14, v24, v14
	v_mul_f32_e32 v11, v25, v15
	v_med3_f32 v14, v14, s75, v233
	v_med3_f32 v11, v11, s75, v233
	v_cvt_pk_fp8_f32 v13, v14, v11 op_sel:[0,0,1]
	v_add_u32_e32 v11, 0x10000, v10
	s_waitcnt lgkmcnt(0)
	global_store_dwordx4 v11, v[2:5], s[16:17] sc1
	ds_write_b64 v8, v[6:7] offset:1024
	ds_write_b64 v8, v[12:13] offset:1536
	ds_read_b128 v[2:5], v9 offset:1024
	v_add_u32_e32 v6, 0x14000, v10
	s_andn2_b64 vcc, exec, s[42:43]
	s_waitcnt lgkmcnt(0)
	global_store_dwordx4 v6, v[2:5], s[16:17] sc1
	s_cbranch_vccnz .LBB0_1856
	s_andn2_b64 vcc, exec, s[20:21]
	s_cbranch_vccnz .LBB0_1823
	s_barrier
	s_branch .LBB0_1823

.LBB0_1974:
	v_pk_mul_f32 v[4:5], v[186:187], v[0:1] op_sel_hi:[1,0]
	v_pk_mul_f32 v[6:7], v[184:185], v[0:1] op_sel_hi:[1,0]
	v_pk_mul_f32 v[10:11], v[180:181], v[0:1] op_sel_hi:[1,0]
	v_med3_f32 v3, v6, s74, v250
	v_med3_f32 v6, v7, s74, v250
	v_med3_f32 v7, v4, s74, v250
	v_mov_b32_e32 v4, v207
	v_med3_f32 v18, v5, s74, v250
	v_cvt_pk_fp8_f32 v4, v3, v6
	v_med3_f32 v3, v10, s74, v250
	v_med3_f32 v6, v11, s74, v250
	v_mov_b32_e32 v5, v207
	v_cvt_pk_fp8_f32 v5, v3, v6
	v_pk_mul_f32 v[8:9], v[182:183], v[0:1] op_sel_hi:[1,0]
	v_pk_mul_f32 v[14:15], v[192:193], v[0:1] op_sel_hi:[1,0]
	v_med3_f32 v3, v8, s74, v250
	v_med3_f32 v6, v9, s74, v250
	v_pk_mul_f32 v[12:13], v[194:195], v[0:1] op_sel_hi:[1,0]
	v_pk_mul_f32 v[16:17], v[190:191], v[0:1] op_sel_hi:[1,0]
	v_pk_mul_f32 v[0:1], v[188:189], v[0:1] op_sel_hi:[1,0]
	v_cvt_pk_fp8_f32 v4, v7, v18 op_sel:[0,0,1]
	v_cvt_pk_fp8_f32 v5, v3, v6 op_sel:[0,0,1]
	v_med3_f32 v3, v14, s74, v250
	v_med3_f32 v7, v15, s74, v250
	v_mov_b32_e32 v6, v207
	v_cvt_pk_fp8_f32 v6, v3, v7
	v_med3_f32 v0, v0, s74, v250
	v_med3_f32 v1, v1, s74, v250
	v_mov_b32_e32 v7, v207
	v_cvt_pk_fp8_f32 v7, v0, v1
	v_med3_f32 v8, v12, s74, v250
	v_med3_f32 v9, v13, s74, v250
	v_med3_f32 v0, v16, s74, v250
	v_med3_f32 v1, v17, s74, v250
	v_cvt_pk_fp8_f32 v6, v8, v9 op_sel:[0,0,1]
	v_cvt_pk_fp8_f32 v7, v0, v1 op_sel:[0,0,1]
	v_add_u32_e32 v0, v232, v236
	v_ashrrev_i32_e32 v1, 31, v0
	v_lshlrev_b64 v[8:9], 11, v[0:1]
	ds_write_b128 v251, v[4:7]
	ds_read_b128 v[4:7], v252
	s_lshl_b32 s40, s40, 8
	v_lshl_add_u64 v[8:9], s[16:17], 0, v[8:9]
	s_ashr_i32 s41, s40, 31
	v_lshl_add_u64 v[8:9], v[8:9], 0, s[40:41]
	v_lshl_add_u64 v[8:9], v[8:9], 0, s[12:13]
	v_cndmask_b32_e64 v1, 0, 1, s[46:47]
	v_lshl_add_u64 v[8:9], v[8:9], 0, v[214:215]
	v_cmp_ne_u32_e64 s[2:3], 1, v1
	s_andn2_b64 vcc, exec, s[46:47]
	s_waitcnt lgkmcnt(0)
	global_store_dwordx4 v[8:9], v[4:7], off sc1
	s_cbranch_vccnz .LBB0_1978
	v_or_b32_e32 v1, 16, v234
	v_cmp_lt_i32_e32 vcc, v1, v233
	s_waitcnt vmcnt(6)
	v_mul_f32_e32 v2, 0.5, v25
	v_cndmask_b32_e32 v2, 0, v2, vcc
.LBB0_1978:
	s_nop 0
	v_pk_mul_f32 v[6:7], v[168:169], v[2:3] op_sel_hi:[1,0]
	v_pk_mul_f32 v[4:5], v[170:171], v[2:3] op_sel_hi:[1,0]
	v_pk_mul_f32 v[8:9], v[166:167], v[2:3] op_sel_hi:[1,0]
	v_pk_mul_f32 v[10:11], v[164:165], v[2:3] op_sel_hi:[1,0]
	v_pk_mul_f32 v[12:13], v[178:179], v[2:3] op_sel_hi:[1,0]
	v_pk_mul_f32 v[14:15], v[176:177], v[2:3] op_sel_hi:[1,0]
	v_pk_mul_f32 v[16:17], v[174:175], v[2:3] op_sel_hi:[1,0]
	v_pk_mul_f32 v[18:19], v[172:173], v[2:3] op_sel_hi:[1,0]
	v_med3_f32 v1, v6, s74, v250
	v_med3_f32 v3, v7, s74, v250
	v_mov_b32_e32 v2, v207
	v_cvt_pk_fp8_f32 v2, v1, v3
	v_med3_f32 v1, v10, s74, v250
	v_med3_f32 v6, v11, s74, v250
	v_mov_b32_e32 v3, v207
	v_cvt_pk_fp8_f32 v3, v1, v6
	v_med3_f32 v4, v4, s74, v250
	v_med3_f32 v5, v5, s74, v250
	v_cvt_pk_fp8_f32 v2, v4, v5 op_sel:[0,0,1]
	v_med3_f32 v1, v8, s74, v250
	v_med3_f32 v4, v9, s74, v250
	v_cvt_pk_fp8_f32 v3, v1, v4 op_sel:[0,0,1]
	v_med3_f32 v1, v14, s74, v250
	v_med3_f32 v5, v15, s74, v250
	v_mov_b32_e32 v4, v207
	v_cvt_pk_fp8_f32 v4, v1, v5
	v_med3_f32 v1, v18, s74, v250
	v_med3_f32 v8, v19, s74, v250
	v_mov_b32_e32 v5, v207
	v_cvt_pk_fp8_f32 v5, v1, v8
	v_med3_f32 v6, v12, s74, v250
	v_med3_f32 v7, v13, s74, v250
	v_cvt_pk_fp8_f32 v4, v6, v7 op_sel:[0,0,1]
	v_med3_f32 v1, v16, s74, v250
	v_med3_f32 v6, v17, s74, v250
	v_cvt_pk_fp8_f32 v5, v1, v6 op_sel:[0,0,1]
	v_or_b32_e32 v1, 16, v236
	v_add_u32_e32 v6, v1, v232
	v_ashrrev_i32_e32 v7, 31, v6
	ds_write_b128 v251, v[2:5] offset:1024
	ds_read_b128 v[2:5], v252 offset:1024
	v_lshlrev_b64 v[6:7], 11, v[6:7]
	v_lshl_add_u64 v[6:7], s[16:17], 0, v[6:7]
	v_lshl_add_u64 v[6:7], v[6:7], 0, s[40:41]
	v_lshl_add_u64 v[6:7], v[6:7], 0, s[12:13]
	v_lshl_add_u64 v[6:7], v[6:7], 0, v[214:215]
	s_waitcnt lgkmcnt(0)
	global_store_dwordx4 v[6:7], v[2:5], off sc1
	s_and_b64 vcc, exec, s[2:3]
	s_nop 0
	v_mov_b32_e32 v2, 0.5
	v_mov_b32_e32 v4, 0.5
	s_cbranch_vccnz .LBB0_1982
	v_or_b32_e32 v1, 32, v234
	v_cmp_lt_i32_e32 vcc, v1, v233
	s_waitcnt vmcnt(5)
	v_mul_f32_e32 v4, 0.5, v26
	v_cndmask_b32_e32 v4, 0, v4, vcc
.LBB0_1982:
	v_pk_mul_f32 v[8:9], v[152:153], v[4:5] op_sel_hi:[1,0]
	v_pk_mul_f32 v[6:7], v[154:155], v[4:5] op_sel_hi:[1,0]
	v_pk_mul_f32 v[10:11], v[150:151], v[4:5] op_sel_hi:[1,0]
	v_pk_mul_f32 v[12:13], v[148:149], v[4:5] op_sel_hi:[1,0]
	v_pk_mul_f32 v[14:15], v[162:163], v[4:5] op_sel_hi:[1,0]
	v_pk_mul_f32 v[16:17], v[160:161], v[4:5] op_sel_hi:[1,0]
	v_pk_mul_f32 v[18:19], v[158:159], v[4:5] op_sel_hi:[1,0]
	v_pk_mul_f32 v[20:21], v[156:157], v[4:5] op_sel_hi:[1,0]
	v_med3_f32 v1, v8, s74, v250
	v_med3_f32 v3, v9, s74, v250
	v_mov_b32_e32 v4, v207
	v_cvt_pk_fp8_f32 v4, v1, v3
	v_med3_f32 v1, v12, s74, v250
	v_med3_f32 v3, v13, s74, v250
	v_mov_b32_e32 v5, v207
	v_cvt_pk_fp8_f32 v5, v1, v3
	v_med3_f32 v6, v6, s74, v250
	v_med3_f32 v7, v7, s74, v250
	v_med3_f32 v1, v10, s74, v250
	v_med3_f32 v3, v11, s74, v250
	v_cvt_pk_fp8_f32 v4, v6, v7 op_sel:[0,0,1]
	v_cvt_pk_fp8_f32 v5, v1, v3 op_sel:[0,0,1]
	v_med3_f32 v1, v16, s74, v250
	v_med3_f32 v3, v17, s74, v250
	v_mov_b32_e32 v6, v207
	v_cvt_pk_fp8_f32 v6, v1, v3
	v_med3_f32 v1, v20, s74, v250
	v_med3_f32 v3, v21, s74, v250
	v_mov_b32_e32 v7, v207
	v_cvt_pk_fp8_f32 v7, v1, v3
	v_med3_f32 v8, v14, s74, v250
	v_med3_f32 v9, v15, s74, v250
	v_med3_f32 v1, v18, s74, v250
	v_med3_f32 v3, v19, s74, v250
	v_cvt_pk_fp8_f32 v6, v8, v9 op_sel:[0,0,1]
	v_cvt_pk_fp8_f32 v7, v1, v3 op_sel:[0,0,1]
	v_add_u32_e32 v8, v239, v232
	v_ashrrev_i32_e32 v9, 31, v8
	v_lshlrev_b64 v[8:9], 11, v[8:9]
	ds_write_b128 v251, v[4:7]
	ds_read_b128 v[4:7], v252
	v_lshl_add_u64 v[8:9], s[16:17], 0, v[8:9]
	v_lshl_add_u64 v[8:9], v[8:9], 0, s[40:41]
	v_lshl_add_u64 v[8:9], v[8:9], 0, s[12:13]
	v_lshl_add_u64 v[8:9], v[8:9], 0, v[214:215]
	s_and_b64 vcc, exec, s[2:3]
	s_waitcnt lgkmcnt(0)
	global_store_dwordx4 v[8:9], v[4:7], off sc1
	s_cbranch_vccnz .LBB0_1986
	v_or_b32_e32 v1, 48, v234
	v_cmp_lt_i32_e32 vcc, v1, v233
	s_waitcnt vmcnt(4)
	v_mul_f32_e32 v2, 0.5, v27
	v_cndmask_b32_e32 v2, 0, v2, vcc
.LBB0_1986:
	s_nop 0
	v_pk_mul_f32 v[6:7], v[120:121], v[2:3] op_sel_hi:[1,0]
	v_pk_mul_f32 v[4:5], v[122:123], v[2:3] op_sel_hi:[1,0]
	v_pk_mul_f32 v[8:9], v[118:119], v[2:3] op_sel_hi:[1,0]
	v_pk_mul_f32 v[10:11], v[116:117], v[2:3] op_sel_hi:[1,0]
	v_pk_mul_f32 v[12:13], v[130:131], v[2:3] op_sel_hi:[1,0]
	v_pk_mul_f32 v[14:15], v[128:129], v[2:3] op_sel_hi:[1,0]
	v_pk_mul_f32 v[16:17], v[126:127], v[2:3] op_sel_hi:[1,0]
	v_pk_mul_f32 v[18:19], v[124:125], v[2:3] op_sel_hi:[1,0]
	v_med3_f32 v1, v6, s74, v250
	v_med3_f32 v3, v7, s74, v250
	v_mov_b32_e32 v2, v207
	v_cvt_pk_fp8_f32 v2, v1, v3
	v_med3_f32 v1, v10, s74, v250
	v_med3_f32 v6, v11, s74, v250
	v_mov_b32_e32 v3, v207
	v_cvt_pk_fp8_f32 v3, v1, v6
	v_med3_f32 v4, v4, s74, v250
	v_med3_f32 v5, v5, s74, v250
	v_cvt_pk_fp8_f32 v2, v4, v5 op_sel:[0,0,1]
	v_med3_f32 v1, v8, s74, v250
	v_med3_f32 v4, v9, s74, v250
	v_cvt_pk_fp8_f32 v3, v1, v4 op_sel:[0,0,1]
	v_med3_f32 v1, v14, s74, v250
	v_med3_f32 v5, v15, s74, v250
	v_mov_b32_e32 v4, v207
	v_cvt_pk_fp8_f32 v4, v1, v5
	v_med3_f32 v1, v18, s74, v250
	v_med3_f32 v8, v19, s74, v250
	v_mov_b32_e32 v5, v207
	v_cvt_pk_fp8_f32 v5, v1, v8
	v_med3_f32 v6, v12, s74, v250
	v_med3_f32 v7, v13, s74, v250
	v_cvt_pk_fp8_f32 v4, v6, v7 op_sel:[0,0,1]
	v_med3_f32 v1, v16, s74, v250
	v_med3_f32 v6, v17, s74, v250
	v_cvt_pk_fp8_f32 v5, v1, v6 op_sel:[0,0,1]
	v_add_u32_e32 v6, v241, v232
	v_ashrrev_i32_e32 v7, 31, v6
	v_lshlrev_b64 v[6:7], 11, v[6:7]
	ds_write_b128 v251, v[2:5] offset:1024
	ds_read_b128 v[2:5], v252 offset:1024
	v_lshl_add_u64 v[6:7], s[16:17], 0, v[6:7]
	v_lshl_add_u64 v[6:7], v[6:7], 0, s[40:41]
	v_lshl_add_u64 v[6:7], v[6:7], 0, s[12:13]
	v_lshl_add_u64 v[6:7], v[6:7], 0, v[214:215]
	s_waitcnt lgkmcnt(0)
	global_store_dwordx4 v[6:7], v[2:5], off sc1
	s_and_b64 vcc, exec, s[2:3]
	s_nop 0
	v_mov_b32_e32 v2, 0.5
	v_mov_b32_e32 v4, 0.5
	s_cbranch_vccnz .LBB0_1990
	v_add_u32_e32 v1, 0x80, v234
	v_cmp_lt_i32_e32 vcc, v1, v233
	s_waitcnt vmcnt(3)
	v_mul_f32_e32 v4, 0.5, v28
	v_cndmask_b32_e32 v4, 0, v4, vcc
.LBB0_1990:
	v_pk_mul_f32 v[8:9], v[136:137], v[4:5] op_sel_hi:[1,0]
	v_pk_mul_f32 v[6:7], v[138:139], v[4:5] op_sel_hi:[1,0]
	v_pk_mul_f32 v[10:11], v[134:135], v[4:5] op_sel_hi:[1,0]
	v_pk_mul_f32 v[12:13], v[132:133], v[4:5] op_sel_hi:[1,0]
	v_pk_mul_f32 v[14:15], v[146:147], v[4:5] op_sel_hi:[1,0]
	v_pk_mul_f32 v[16:17], v[144:145], v[4:5] op_sel_hi:[1,0]
	v_pk_mul_f32 v[18:19], v[142:143], v[4:5] op_sel_hi:[1,0]
	v_pk_mul_f32 v[20:21], v[140:141], v[4:5] op_sel_hi:[1,0]
	v_med3_f32 v1, v8, s74, v250
	v_med3_f32 v3, v9, s74, v250
	v_mov_b32_e32 v4, v207
	v_cvt_pk_fp8_f32 v4, v1, v3
	v_med3_f32 v1, v12, s74, v250
	v_med3_f32 v3, v13, s74, v250
	v_mov_b32_e32 v5, v207
	v_cvt_pk_fp8_f32 v5, v1, v3
	v_med3_f32 v6, v6, s74, v250
	v_med3_f32 v7, v7, s74, v250
	v_med3_f32 v1, v10, s74, v250
	v_med3_f32 v3, v11, s74, v250
	v_cvt_pk_fp8_f32 v4, v6, v7 op_sel:[0,0,1]
	v_cvt_pk_fp8_f32 v5, v1, v3 op_sel:[0,0,1]
	v_med3_f32 v1, v16, s74, v250
	v_med3_f32 v3, v17, s74, v250
	v_mov_b32_e32 v6, v207
	v_cvt_pk_fp8_f32 v6, v1, v3
	v_med3_f32 v1, v20, s74, v250
	v_med3_f32 v3, v21, s74, v250
	v_mov_b32_e32 v7, v207
	v_cvt_pk_fp8_f32 v7, v1, v3
	v_med3_f32 v8, v14, s74, v250
	v_med3_f32 v9, v15, s74, v250
	v_med3_f32 v1, v18, s74, v250
	v_med3_f32 v3, v19, s74, v250
	v_cvt_pk_fp8_f32 v6, v8, v9 op_sel:[0,0,1]
	v_cvt_pk_fp8_f32 v7, v1, v3 op_sel:[0,0,1]
	v_add_u32_e32 v8, 0x80, v0
	v_ashrrev_i32_e32 v9, 31, v8
	v_lshlrev_b64 v[8:9], 11, v[8:9]
	ds_write_b128 v251, v[4:7]
	ds_read_b128 v[4:7], v252
	v_lshl_add_u64 v[8:9], s[16:17], 0, v[8:9]
	v_lshl_add_u64 v[8:9], v[8:9], 0, s[40:41]
	v_lshl_add_u64 v[8:9], v[8:9], 0, s[12:13]
	v_lshl_add_u64 v[8:9], v[8:9], 0, v[214:215]
	s_and_b64 vcc, exec, s[2:3]
	s_waitcnt lgkmcnt(0)
	global_store_dwordx4 v[8:9], v[4:7], off sc1
	s_cbranch_vccnz .LBB0_1994
	v_add_u32_e32 v1, 0x90, v234
	v_cmp_lt_i32_e32 vcc, v1, v233
	s_waitcnt vmcnt(2)
	v_mul_f32_e32 v2, 0.5, v29
	v_cndmask_b32_e32 v2, 0, v2, vcc
.LBB0_1994:
	s_nop 0
	v_pk_mul_f32 v[6:7], v[104:105], v[2:3] op_sel_hi:[1,0]
	v_pk_mul_f32 v[4:5], v[106:107], v[2:3] op_sel_hi:[1,0]
	v_pk_mul_f32 v[8:9], v[102:103], v[2:3] op_sel_hi:[1,0]
	v_pk_mul_f32 v[10:11], v[100:101], v[2:3] op_sel_hi:[1,0]
	v_pk_mul_f32 v[12:13], v[114:115], v[2:3] op_sel_hi:[1,0]
	v_pk_mul_f32 v[14:15], v[112:113], v[2:3] op_sel_hi:[1,0]
	v_pk_mul_f32 v[16:17], v[110:111], v[2:3] op_sel_hi:[1,0]
	v_pk_mul_f32 v[18:19], v[108:109], v[2:3] op_sel_hi:[1,0]
	v_med3_f32 v1, v6, s74, v250
	v_med3_f32 v3, v7, s74, v250
	v_mov_b32_e32 v2, v207
	v_cvt_pk_fp8_f32 v2, v1, v3
	v_med3_f32 v1, v10, s74, v250
	v_med3_f32 v6, v11, s74, v250
	v_mov_b32_e32 v3, v207
	v_cvt_pk_fp8_f32 v3, v1, v6
	v_med3_f32 v4, v4, s74, v250
	v_med3_f32 v5, v5, s74, v250
	v_cvt_pk_fp8_f32 v2, v4, v5 op_sel:[0,0,1]
	v_med3_f32 v1, v8, s74, v250
	v_med3_f32 v4, v9, s74, v250
	v_cvt_pk_fp8_f32 v3, v1, v4 op_sel:[0,0,1]
	v_med3_f32 v1, v14, s74, v250
	v_med3_f32 v5, v15, s74, v250
	v_mov_b32_e32 v4, v207
	v_cvt_pk_fp8_f32 v4, v1, v5
	v_med3_f32 v1, v18, s74, v250
	v_med3_f32 v8, v19, s74, v250
	v_mov_b32_e32 v5, v207
	v_cvt_pk_fp8_f32 v5, v1, v8
	v_med3_f32 v6, v12, s74, v250
	v_med3_f32 v7, v13, s74, v250
	v_cvt_pk_fp8_f32 v4, v6, v7 op_sel:[0,0,1]
	v_med3_f32 v1, v16, s74, v250
	v_med3_f32 v6, v17, s74, v250
	v_cvt_pk_fp8_f32 v5, v1, v6 op_sel:[0,0,1]
	v_add_u32_e32 v6, 0x90, v0
	v_ashrrev_i32_e32 v7, 31, v6
	v_lshlrev_b64 v[6:7], 11, v[6:7]
	ds_write_b128 v251, v[2:5] offset:1024
	ds_read_b128 v[2:5], v252 offset:1024
	v_lshl_add_u64 v[6:7], s[16:17], 0, v[6:7]
	v_lshl_add_u64 v[6:7], v[6:7], 0, s[40:41]
	v_lshl_add_u64 v[6:7], v[6:7], 0, s[12:13]
	v_lshl_add_u64 v[6:7], v[6:7], 0, v[214:215]
	s_waitcnt lgkmcnt(0)
	global_store_dwordx4 v[6:7], v[2:5], off sc1
	s_and_b64 vcc, exec, s[2:3]
	s_nop 0
	v_mov_b32_e32 v2, 0.5
	v_mov_b32_e32 v4, 0.5
	s_cbranch_vccnz .LBB0_1998
	v_cmp_lt_i32_e32 vcc, v244, v233
	s_waitcnt vmcnt(1)
	v_mul_f32_e32 v4, 0.5, v30
	v_cndmask_b32_e32 v4, 0, v4, vcc
.LBB0_1998:
	v_pk_mul_f32 v[8:9], v[88:89], v[4:5] op_sel_hi:[1,0]
	v_pk_mul_f32 v[6:7], v[90:91], v[4:5] op_sel_hi:[1,0]
	v_pk_mul_f32 v[10:11], v[86:87], v[4:5] op_sel_hi:[1,0]
	v_pk_mul_f32 v[12:13], v[84:85], v[4:5] op_sel_hi:[1,0]
	v_pk_mul_f32 v[14:15], v[98:99], v[4:5] op_sel_hi:[1,0]
	v_pk_mul_f32 v[16:17], v[96:97], v[4:5] op_sel_hi:[1,0]
	v_pk_mul_f32 v[18:19], v[94:95], v[4:5] op_sel_hi:[1,0]
	v_pk_mul_f32 v[20:21], v[92:93], v[4:5] op_sel_hi:[1,0]
	v_med3_f32 v1, v8, s74, v250
	v_med3_f32 v3, v9, s74, v250
	v_mov_b32_e32 v4, v207
	v_cvt_pk_fp8_f32 v4, v1, v3
	v_med3_f32 v1, v12, s74, v250
	v_med3_f32 v3, v13, s74, v250
	v_mov_b32_e32 v5, v207
	v_cvt_pk_fp8_f32 v5, v1, v3
	v_med3_f32 v6, v6, s74, v250
	v_med3_f32 v7, v7, s74, v250
	v_med3_f32 v1, v10, s74, v250
	v_med3_f32 v3, v11, s74, v250
	v_cvt_pk_fp8_f32 v4, v6, v7 op_sel:[0,0,1]
	v_cvt_pk_fp8_f32 v5, v1, v3 op_sel:[0,0,1]
	v_med3_f32 v1, v16, s74, v250
	v_med3_f32 v3, v17, s74, v250
	v_mov_b32_e32 v6, v207
	v_cvt_pk_fp8_f32 v6, v1, v3
	v_med3_f32 v1, v20, s74, v250
	v_med3_f32 v3, v21, s74, v250
	v_mov_b32_e32 v7, v207
	v_cvt_pk_fp8_f32 v7, v1, v3
	v_med3_f32 v8, v14, s74, v250
	v_med3_f32 v9, v15, s74, v250
	v_med3_f32 v1, v18, s74, v250
	v_med3_f32 v3, v19, s74, v250
	v_cvt_pk_fp8_f32 v6, v8, v9 op_sel:[0,0,1]
	v_cvt_pk_fp8_f32 v7, v1, v3 op_sel:[0,0,1]
	v_add_u32_e32 v8, 0xa0, v0
	v_ashrrev_i32_e32 v9, 31, v8
	v_lshlrev_b64 v[8:9], 11, v[8:9]
	ds_write_b128 v251, v[4:7]
	ds_read_b128 v[4:7], v252
	v_lshl_add_u64 v[8:9], s[16:17], 0, v[8:9]
	v_lshl_add_u64 v[8:9], v[8:9], 0, s[40:41]
	v_lshl_add_u64 v[8:9], v[8:9], 0, s[12:13]
	v_lshl_add_u64 v[8:9], v[8:9], 0, v[214:215]
	s_and_b64 vcc, exec, s[2:3]
	s_waitcnt lgkmcnt(0)
	global_store_dwordx4 v[8:9], v[4:7], off sc1
	s_cbranch_vccnz .LBB0_2002
	v_cmp_lt_i32_e32 vcc, v245, v233
	s_waitcnt vmcnt(0)
	v_mul_f32_e32 v2, 0.5, v31
	v_cndmask_b32_e32 v2, 0, v2, vcc
.LBB0_2002:
	s_nop 0
	v_pk_mul_f32 v[6:7], v[76:77], v[2:3] op_sel_hi:[1,0]
	v_pk_mul_f32 v[4:5], v[78:79], v[2:3] op_sel_hi:[1,0]
	v_pk_mul_f32 v[8:9], v[74:75], v[2:3] op_sel_hi:[1,0]
	v_pk_mul_f32 v[10:11], v[72:73], v[2:3] op_sel_hi:[1,0]
	v_pk_mul_f32 v[12:13], v[82:83], v[2:3] op_sel_hi:[1,0]
	v_pk_mul_f32 v[14:15], v[80:81], v[2:3] op_sel_hi:[1,0]
	v_pk_mul_f32 v[16:17], v[70:71], v[2:3] op_sel_hi:[1,0]
	v_pk_mul_f32 v[18:19], v[68:69], v[2:3] op_sel_hi:[1,0]
	v_med3_f32 v1, v6, s74, v250
	v_med3_f32 v3, v7, s74, v250
	v_mov_b32_e32 v2, v207
	v_cvt_pk_fp8_f32 v2, v1, v3
	v_med3_f32 v1, v10, s74, v250
	v_med3_f32 v6, v11, s74, v250
	v_mov_b32_e32 v3, v207
	v_cvt_pk_fp8_f32 v3, v1, v6
	v_med3_f32 v4, v4, s74, v250
	v_med3_f32 v5, v5, s74, v250
	v_cvt_pk_fp8_f32 v2, v4, v5 op_sel:[0,0,1]
	v_med3_f32 v1, v8, s74, v250
	v_med3_f32 v4, v9, s74, v250
	v_cvt_pk_fp8_f32 v3, v1, v4 op_sel:[0,0,1]
	v_med3_f32 v1, v14, s74, v250
	v_med3_f32 v5, v15, s74, v250
	v_mov_b32_e32 v4, v207
	v_cvt_pk_fp8_f32 v4, v1, v5
	v_med3_f32 v1, v18, s74, v250
	v_med3_f32 v8, v19, s74, v250
	v_mov_b32_e32 v5, v207
	v_cvt_pk_fp8_f32 v5, v1, v8
	v_med3_f32 v6, v12, s74, v250
	v_med3_f32 v7, v13, s74, v250
	v_cvt_pk_fp8_f32 v4, v6, v7 op_sel:[0,0,1]
	v_med3_f32 v1, v16, s74, v250
	v_med3_f32 v6, v17, s74, v250
	v_cvt_pk_fp8_f32 v5, v1, v6 op_sel:[0,0,1]
	v_add_u32_e32 v0, 0xb0, v0
	v_ashrrev_i32_e32 v1, 31, v0
	v_lshlrev_b64 v[0:1], 11, v[0:1]
	ds_write_b128 v251, v[2:5] offset:1024
	ds_read_b128 v[2:5], v252 offset:1024
	v_lshl_add_u64 v[0:1], s[16:17], 0, v[0:1]
	v_lshl_add_u64 v[0:1], v[0:1], 0, s[40:41]
	v_lshl_add_u64 v[0:1], v[0:1], 0, s[12:13]
	v_lshl_add_u64 v[0:1], v[0:1], 0, v[214:215]
	s_and_b64 vcc, exec, s[0:1]
	s_mov_b64 s[0:1], -1
	s_waitcnt lgkmcnt(0)
	global_store_dwordx4 v[0:1], v[2:5], off sc1
	s_cbranch_vccnz .LBB0_1942
	s_andn2_b64 vcc, exec, s[14:15]
	s_cbranch_vccnz .LBB0_1941
	s_barrier
	s_branch .LBB0_1941
